# GEMM K-loops: redundant post-barrier lgkmcnt(0) dropped and s_setprio 1 moved ahead of the barrier (36 segments)
# speedup vs baseline: 1.0021x; 1.0003x over previous
.LBB0_177:
	s_add_u32 s28, s4, s26
	s_addc_u32 s29, s5, s27
	s_add_u32 s30, s28, 0xe000100
	s_addc_u32 s31, s29, 0
	ds_read_b128 v[24:27], v252
	ds_read_b128 v[28:31], v253
	s_and_b64 s[28:29], s[34:35], exec
	ds_read_b128 v[16:19], v252 offset:2048
	ds_read_b128 v[20:23], v253 offset:2048
	s_cselect_b32 s29, s7, s31
	s_cselect_b32 s28, s6, s30
	s_add_u32 s61, s56, s26
	ds_read_b128 v[8:11], v252 offset:16384
	ds_read_b128 v[12:15], v253 offset:16384
	s_addc_u32 s62, s57, s27
	ds_read_b128 v[0:3], v252 offset:18432
	ds_read_b128 v[4:7], v253 offset:18432
	s_and_b64 s[30:31], s[34:35], exec
	s_cselect_b32 s31, s23, s62
	s_cselect_b32 s30, s22, s61
	s_add_u32 s61, s58, s26
	s_addc_u32 s62, s59, s27
	s_and_b64 s[34:35], s[34:35], exec
	s_cselect_b32 s35, s25, s62
	s_cselect_b32 s34, s24, s61
	s_add_u32 s100, s16, s26
	s_addc_u32 s101, s17, s27
	s_add_i32 m0, s37, 0xc000
	ds_read_b128 v[186:189], v206
	ds_read_b128 v[214:217], v206 offset:2048
	ds_read_b128 v[190:193], v207
	ds_read_b128 v[218:221], v207 offset:2048
	ds_read_b128 v[222:225], v206 offset:4096
	ds_read_b128 v[230:233], v206 offset:6144
	ds_read_b128 v[226:229], v207 offset:4096
	ds_read_b128 v[234:237], v207 offset:6144
	global_load_lds_dwordx4 v166, s[100:101]
	s_add_i32 m0, s37, 0xe000
	s_nop 0
	global_load_lds_dwordx4 v168, s[100:101]
	s_waitcnt vmcnt(8)
	s_waitcnt lgkmcnt(0)
	s_setprio 1
	s_barrier
	s_cmp_eq_u32 s26, 0
	s_cbranch_scc1 .Lc0_P2_0
	v_mfma_f32_16x16x128_f8f6f4 v[156:159], v[24:31], v[186:193], v[156:159]
	v_mfma_f32_16x16x128_f8f6f4 v[152:155], v[16:23], v[186:193], v[152:155]
	v_mfma_f32_16x16x128_f8f6f4 v[136:139], v[16:23], v[214:221], v[136:139]
	v_mfma_f32_16x16x128_f8f6f4 v[144:147], v[24:31], v[214:221], v[144:147]
	v_mfma_f32_16x16x128_f8f6f4 v[128:131], v[24:31], v[222:229], v[128:131]
	v_mfma_f32_16x16x128_f8f6f4 v[120:123], v[16:23], v[222:229], v[120:123]
	v_mfma_f32_16x16x128_f8f6f4 v[104:107], v[16:23], v[230:237], v[104:107]
	v_mfma_f32_16x16x128_f8f6f4 v[112:115], v[24:31], v[230:237], v[112:115]
	v_mfma_f32_16x16x128_f8f6f4 v[148:151], v[8:15], v[186:193], v[148:151]
	v_mfma_f32_16x16x128_f8f6f4 v[140:143], v[0:7], v[186:193], v[140:143]
	v_mfma_f32_16x16x128_f8f6f4 v[124:127], v[0:7], v[214:221], v[124:127]
	v_mfma_f32_16x16x128_f8f6f4 v[132:135], v[8:15], v[214:221], v[132:135]
	v_mfma_f32_16x16x128_f8f6f4 v[116:119], v[8:15], v[222:229], v[116:119]
	v_mfma_f32_16x16x128_f8f6f4 v[108:111], v[0:7], v[222:229], v[108:111]
	v_mfma_f32_16x16x128_f8f6f4 v[96:99], v[0:7], v[230:237], v[96:99]
	v_mfma_f32_16x16x128_f8f6f4 v[100:103], v[8:15], v[230:237], v[100:103]
.Lc0b_P2_0:
	s_setprio 0
	s_barrier
	s_add_i32 s61, s44, s36
	s_mov_b32 m0, s61
	ds_read_b128 v[214:217], v206 offset:16384
	ds_read_b128 v[222:225], v206 offset:18432
	ds_read_b128 v[218:221], v207 offset:16384
	ds_read_b128 v[226:229], v207 offset:18432
	ds_read_b128 v[230:233], v206 offset:20480
	ds_read_b128 v[238:241], v206 offset:22528
	ds_read_b128 v[234:237], v207 offset:20480
	ds_read_b128 v[242:245], v207 offset:22528
	global_load_lds_dwordx4 v160, s[30:31]
	s_add_i32 m0, s61, 0x2000
	s_add_i32 s98, s46, s36
	global_load_lds_dwordx4 v162, s[30:31]
	s_mov_b32 m0, s98
	s_nop 0
	global_load_lds_dwordx4 v160, s[34:35]
	s_add_i32 m0, s98, 0x2000
	v_mov_b32_e32 v173, v165
	global_load_lds_dwordx4 v162, s[34:35]
	s_waitcnt vmcnt(6)
	s_waitcnt lgkmcnt(0)
	s_setprio 1
	s_barrier
	s_cmp_eq_u32 s26, 0
	s_cbranch_scc1 .Lc0_P2_1
	v_mfma_f32_16x16x128_f8f6f4 v[92:95], v[24:31], v[214:221], v[92:95]
	v_mfma_f32_16x16x128_f8f6f4 v[88:91], v[16:23], v[214:221], v[88:91]
	v_mfma_f32_16x16x128_f8f6f4 v[72:75], v[16:23], v[222:229], v[72:75]
	v_mfma_f32_16x16x128_f8f6f4 v[80:83], v[24:31], v[222:229], v[80:83]
	s_mov_b32 m0, s37
	v_mfma_f32_16x16x128_f8f6f4 v[64:67], v[24:31], v[230:237], v[64:67]
	global_load_lds_dwordx4 v164, s[28:29]
	v_mfma_f32_16x16x128_f8f6f4 v[56:59], v[16:23], v[230:237], v[56:59]
	v_mfma_f32_16x16x128_f8f6f4 v[40:43], v[16:23], v[238:245], v[40:43]
	v_mfma_f32_16x16x128_f8f6f4 v[48:51], v[24:31], v[238:245], v[48:51]
	v_mfma_f32_16x16x128_f8f6f4 v[84:87], v[8:15], v[214:221], v[84:87]
	s_mov_b32 m0, s38
	v_mfma_f32_16x16x128_f8f6f4 v[76:79], v[0:7], v[214:221], v[76:79]
	global_load_lds_dwordx4 v172, s[28:29]
	v_mfma_f32_16x16x128_f8f6f4 v[60:63], v[0:7], v[222:229], v[60:63]
	v_mfma_f32_16x16x128_f8f6f4 v[68:71], v[8:15], v[222:229], v[68:71]
	v_mfma_f32_16x16x128_f8f6f4 v[52:55], v[8:15], v[230:237], v[52:55]
	v_mfma_f32_16x16x128_f8f6f4 v[44:47], v[0:7], v[230:237], v[44:47]
	v_mfma_f32_16x16x128_f8f6f4 v[32:35], v[0:7], v[238:245], v[32:35]
	v_mfma_f32_16x16x128_f8f6f4 v[36:39], v[8:15], v[238:245], v[36:39]
.Lc0b_P2_1:
	s_setprio 0
	s_barrier
	ds_read_b128 v[0:3], v252 offset:32768
	ds_read_b128 v[4:7], v253 offset:32768
	ds_read_b128 v[8:11], v252 offset:34816
	ds_read_b128 v[12:15], v253 offset:34816
	ds_read_b128 v[16:19], v252 offset:49152
	ds_read_b128 v[20:23], v253 offset:49152
	ds_read_b128 v[24:27], v252 offset:51200
	ds_read_b128 v[28:31], v253 offset:51200
	s_mov_b32 m0, s39
	ds_read_b128 v[214:217], v206 offset:32768
	ds_read_b128 v[222:225], v206 offset:34816
	ds_read_b128 v[218:221], v207 offset:32768
	ds_read_b128 v[226:229], v207 offset:34816
	ds_read_b128 v[230:233], v206 offset:36864
	ds_read_b128 v[238:241], v206 offset:38912
	ds_read_b128 v[234:237], v207 offset:36864
	ds_read_b128 v[242:245], v207 offset:38912
	global_load_lds_dwordx4 v184, s[28:29]
	s_mov_b32 m0, s40
	s_nop 0
	global_load_lds_dwordx4 v182, s[28:29]
	s_waitcnt vmcnt(8)
	s_waitcnt lgkmcnt(0)
	s_setprio 1
	s_barrier
	v_mfma_f32_16x16x128_f8f6f4 v[156:159], v[0:7], v[214:221], v[156:159]
	v_mfma_f32_16x16x128_f8f6f4 v[152:155], v[8:15], v[214:221], v[152:155]
	v_mfma_f32_16x16x128_f8f6f4 v[136:139], v[8:15], v[222:229], v[136:139]
	v_mfma_f32_16x16x128_f8f6f4 v[144:147], v[0:7], v[222:229], v[144:147]
	v_mfma_f32_16x16x128_f8f6f4 v[128:131], v[0:7], v[230:237], v[128:131]
	v_mfma_f32_16x16x128_f8f6f4 v[120:123], v[8:15], v[230:237], v[120:123]
	v_mfma_f32_16x16x128_f8f6f4 v[104:107], v[8:15], v[238:245], v[104:107]
	v_mfma_f32_16x16x128_f8f6f4 v[112:115], v[0:7], v[238:245], v[112:115]
	v_mfma_f32_16x16x128_f8f6f4 v[148:151], v[16:23], v[214:221], v[148:151]
	v_mfma_f32_16x16x128_f8f6f4 v[140:143], v[24:31], v[214:221], v[140:143]
	v_mfma_f32_16x16x128_f8f6f4 v[124:127], v[24:31], v[222:229], v[124:127]
	v_mfma_f32_16x16x128_f8f6f4 v[132:135], v[16:23], v[222:229], v[132:135]
	v_mfma_f32_16x16x128_f8f6f4 v[116:119], v[16:23], v[230:237], v[116:119]
	v_mfma_f32_16x16x128_f8f6f4 v[108:111], v[24:31], v[230:237], v[108:111]
	v_mfma_f32_16x16x128_f8f6f4 v[96:99], v[24:31], v[238:245], v[96:99]
	v_mfma_f32_16x16x128_f8f6f4 v[100:103], v[16:23], v[238:245], v[100:103]
	s_setprio 0
	s_barrier
	s_add_i32 s99, s36, 0x17f80
	s_mov_b32 m0, s99
	ds_read_b128 v[214:217], v206 offset:49152
	ds_read_b128 v[222:225], v206 offset:51200
	ds_read_b128 v[218:221], v207 offset:49152
	ds_read_b128 v[226:229], v207 offset:51200
	ds_read_b128 v[230:233], v206 offset:53248
	ds_read_b128 v[238:241], v206 offset:55296
	ds_read_b128 v[234:237], v207 offset:53248
	ds_read_b128 v[242:245], v207 offset:55296
	global_load_lds_dwordx4 v160, s[30:31] offset:128
	s_add_i32 m0, s99, 0x2000
	s_add_i32 s99, s36, 0x1bf80
	global_load_lds_dwordx4 v162, s[30:31] offset:128
	s_mov_b32 m0, s99
	s_nop 0
	global_load_lds_dwordx4 v160, s[34:35] offset:128
	s_add_i32 m0, s99, 0x2000
	s_nop 0
	global_load_lds_dwordx4 v162, s[34:35] offset:128
	s_waitcnt vmcnt(6)
	s_waitcnt lgkmcnt(0)
	s_setprio 1
	s_barrier
	v_mfma_f32_16x16x128_f8f6f4 v[92:95], v[0:7], v[214:221], v[92:95]
	v_mfma_f32_16x16x128_f8f6f4 v[88:91], v[8:15], v[214:221], v[88:91]
	v_mfma_f32_16x16x128_f8f6f4 v[72:75], v[8:15], v[222:229], v[72:75]
	v_mfma_f32_16x16x128_f8f6f4 v[80:83], v[0:7], v[222:229], v[80:83]
	s_add_i32 m0, s41, 0xffffff80
	v_mfma_f32_16x16x128_f8f6f4 v[64:67], v[0:7], v[230:237], v[64:67]
	global_load_lds_dwordx4 v164, s[28:29] offset:128
	v_mfma_f32_16x16x128_f8f6f4 v[56:59], v[8:15], v[230:237], v[56:59]
	v_mfma_f32_16x16x128_f8f6f4 v[40:43], v[8:15], v[238:245], v[40:43]
	v_mfma_f32_16x16x128_f8f6f4 v[48:51], v[0:7], v[238:245], v[48:51]
	v_mfma_f32_16x16x128_f8f6f4 v[84:87], v[16:23], v[214:221], v[84:87]
	s_add_i32 m0, s42, 0xffffff80
	v_mfma_f32_16x16x128_f8f6f4 v[76:79], v[24:31], v[214:221], v[76:79]
	global_load_lds_dwordx4 v172, s[28:29] offset:128
	v_mfma_f32_16x16x128_f8f6f4 v[60:63], v[24:31], v[222:229], v[60:63]
	v_mfma_f32_16x16x128_f8f6f4 v[68:71], v[16:23], v[222:229], v[68:71]
	v_mfma_f32_16x16x128_f8f6f4 v[52:55], v[16:23], v[230:237], v[52:55]
	v_mfma_f32_16x16x128_f8f6f4 v[44:47], v[24:31], v[230:237], v[44:47]
	v_mfma_f32_16x16x128_f8f6f4 v[32:35], v[24:31], v[238:245], v[32:35]
	v_mfma_f32_16x16x128_f8f6f4 v[36:39], v[16:23], v[238:245], v[36:39]
	s_setprio 0
	s_barrier
	s_add_i32 s60, s60, 2
	s_add_u32 s26, s26, 0x100
	s_addc_u32 s27, s27, 0
	s_cmp_gt_u32 s60, 5
	s_cbranch_scc1 .LBB0_180

.LBB0_430:
	s_add_u32 s26, s4, s24
	s_addc_u32 s27, s5, s25
	s_add_u32 s30, s26, 0x21c00100
	s_addc_u32 s31, s27, 0
	ds_read_b128 v[172:175], v252
	ds_read_b128 v[176:179], v253
	s_and_b64 s[26:27], s[28:29], exec
	ds_read_b128 v[180:183], v252 offset:2048
	ds_read_b128 v[184:187], v253 offset:2048
	s_cselect_b32 s27, s7, s31
	s_cselect_b32 s26, s6, s30
	s_add_u32 s65, s60, s24
	ds_read_b128 v[188:191], v252 offset:16384
	ds_read_b128 v[192:195], v253 offset:16384
	s_addc_u32 s66, s61, s25
	ds_read_b128 v[196:199], v252 offset:18432
	ds_read_b128 v[200:203], v253 offset:18432
	s_and_b64 s[30:31], s[28:29], exec
	s_cselect_b32 s31, s21, s66
	s_cselect_b32 s30, s20, s65
	s_add_u32 s65, s62, s24
	s_addc_u32 s66, s63, s25
	s_and_b64 s[28:29], s[28:29], exec
	s_cselect_b32 s29, s23, s66
	s_cselect_b32 s28, s22, s65
	v_lshl_add_u64 v[236:237], v[156:157], 0, s[24:25]
	s_add_i32 m0, s37, 0xc000
	ds_read_b128 v[204:207], v169
	ds_read_b128 v[208:211], v169 offset:1024
	ds_read_b128 v[212:215], v169 offset:2048
	ds_read_b128 v[216:219], v169 offset:3072
	ds_read_b128 v[220:223], v169 offset:4096
	ds_read_b128 v[224:227], v169 offset:5120
	ds_read_b128 v[228:231], v169 offset:6144
	ds_read_b128 v[232:235], v169 offset:7168
	global_load_lds_dwordx4 v[236:237], off
	v_lshl_add_u64 v[236:237], v[154:155], 0, s[24:25]
	s_add_i32 m0, s37, 0xe000
	s_nop 0
	global_load_lds_dwordx4 v[236:237], off
	s_waitcnt vmcnt(8)
	s_waitcnt lgkmcnt(0)
	s_setprio 1
	s_barrier
	v_mfma_f32_16x16x32_bf16 v[140:143], v[172:175], v[204:207], v[140:143]
	v_mfma_f32_16x16x32_bf16 v[136:139], v[180:183], v[204:207], v[136:139]
	v_mfma_f32_16x16x32_bf16 v[124:127], v[172:175], v[212:215], v[124:127]
	v_mfma_f32_16x16x32_bf16 v[120:123], v[180:183], v[212:215], v[120:123]
	v_mfma_f32_16x16x32_bf16 v[92:95], v[172:175], v[220:223], v[92:95]
	v_mfma_f32_16x16x32_bf16 v[88:91], v[180:183], v[220:223], v[88:91]
	v_mfma_f32_16x16x32_bf16 v[76:79], v[172:175], v[228:231], v[76:79]
	v_mfma_f32_16x16x32_bf16 v[72:75], v[180:183], v[228:231], v[72:75]
	v_mfma_f32_16x16x32_bf16 v[140:143], v[176:179], v[208:211], v[140:143]
	v_mfma_f32_16x16x32_bf16 v[136:139], v[184:187], v[208:211], v[136:139]
	v_mfma_f32_16x16x32_bf16 v[124:127], v[176:179], v[216:219], v[124:127]
	v_mfma_f32_16x16x32_bf16 v[120:123], v[184:187], v[216:219], v[120:123]
	v_mfma_f32_16x16x32_bf16 v[92:95], v[176:179], v[224:227], v[92:95]
	v_mfma_f32_16x16x32_bf16 v[88:91], v[184:187], v[224:227], v[88:91]
	v_mfma_f32_16x16x32_bf16 v[76:79], v[176:179], v[232:235], v[76:79]
	v_mfma_f32_16x16x32_bf16 v[72:75], v[184:187], v[232:235], v[72:75]
	v_mfma_f32_16x16x32_bf16 v[132:135], v[188:191], v[204:207], v[132:135]
	v_mfma_f32_16x16x32_bf16 v[128:131], v[196:199], v[204:207], v[128:131]
	v_mfma_f32_16x16x32_bf16 v[108:111], v[188:191], v[212:215], v[108:111]
	v_mfma_f32_16x16x32_bf16 v[96:99], v[196:199], v[212:215], v[96:99]
	v_mfma_f32_16x16x32_bf16 v[84:87], v[188:191], v[220:223], v[84:87]
	v_mfma_f32_16x16x32_bf16 v[80:83], v[196:199], v[220:223], v[80:83]
	v_mfma_f32_16x16x32_bf16 v[68:71], v[188:191], v[228:231], v[68:71]
	v_mfma_f32_16x16x32_bf16 v[64:67], v[196:199], v[228:231], v[64:67]
	v_mfma_f32_16x16x32_bf16 v[132:135], v[192:195], v[208:211], v[132:135]
	v_mfma_f32_16x16x32_bf16 v[128:131], v[200:203], v[208:211], v[128:131]
	v_mfma_f32_16x16x32_bf16 v[108:111], v[192:195], v[216:219], v[108:111]
	v_mfma_f32_16x16x32_bf16 v[96:99], v[200:203], v[216:219], v[96:99]
	v_mfma_f32_16x16x32_bf16 v[84:87], v[192:195], v[224:227], v[84:87]
	v_mfma_f32_16x16x32_bf16 v[80:83], v[200:203], v[224:227], v[80:83]
	v_mfma_f32_16x16x32_bf16 v[68:71], v[192:195], v[232:235], v[68:71]
	v_mfma_f32_16x16x32_bf16 v[64:67], v[200:203], v[232:235], v[64:67]
	s_setprio 0
	s_barrier
	s_add_i32 s65, s48, s35
	v_lshl_add_u64 v[236:237], s[30:31], 0, v[146:147]
	s_mov_b32 m0, s65
	ds_read_b128 v[204:207], v169 offset:16384
	ds_read_b128 v[208:211], v169 offset:17408
	ds_read_b128 v[212:215], v169 offset:18432
	ds_read_b128 v[216:219], v169 offset:19456
	ds_read_b128 v[220:223], v169 offset:20480
	ds_read_b128 v[224:227], v169 offset:21504
	ds_read_b128 v[228:231], v169 offset:22528
	ds_read_b128 v[232:235], v169 offset:23552
	global_load_lds_dwordx4 v[236:237], off
	v_lshl_add_u64 v[238:239], s[30:31], 0, v[148:149]
	s_add_i32 m0, s65, 0x2000
	s_add_i32 s30, s50, s35
	global_load_lds_dwordx4 v[238:239], off
	v_lshl_add_u64 v[240:241], s[28:29], 0, v[146:147]
	s_mov_b32 m0, s30
	v_lshl_add_u64 v[242:243], s[28:29], 0, v[148:149]
	global_load_lds_dwordx4 v[240:241], off
	s_add_i32 m0, s30, 0x2000
	v_mov_b32_e32 v153, v151
	global_load_lds_dwordx4 v[242:243], off
	s_mov_b32 m0, s37
	v_lshl_add_u64 v[244:245], s[26:27], 0, v[150:151]
	global_load_lds_dwordx4 v150, s[26:27]
	s_mov_b32 m0, s38
	v_lshl_add_u64 v[246:247], s[26:27], 0, v[152:153]
	global_load_lds_dwordx4 v152, s[26:27]
	s_waitcnt vmcnt(8)
	s_waitcnt lgkmcnt(0)
	s_setprio 1
	s_barrier
	v_mfma_f32_16x16x32_bf16 v[60:63], v[172:175], v[204:207], v[60:63]
	v_mfma_f32_16x16x32_bf16 v[56:59], v[180:183], v[204:207], v[56:59]
	v_mfma_f32_16x16x32_bf16 v[44:47], v[172:175], v[212:215], v[44:47]
	v_mfma_f32_16x16x32_bf16 v[40:43], v[180:183], v[212:215], v[40:43]
	v_mfma_f32_16x16x32_bf16 v[28:31], v[172:175], v[220:223], v[28:31]
	v_mfma_f32_16x16x32_bf16 v[24:27], v[180:183], v[220:223], v[24:27]
	v_mfma_f32_16x16x32_bf16 v[12:15], v[172:175], v[228:231], v[12:15]
	v_mfma_f32_16x16x32_bf16 v[8:11], v[180:183], v[228:231], v[8:11]
	v_mfma_f32_16x16x32_bf16 v[60:63], v[176:179], v[208:211], v[60:63]
	v_mfma_f32_16x16x32_bf16 v[56:59], v[184:187], v[208:211], v[56:59]
	v_mfma_f32_16x16x32_bf16 v[44:47], v[176:179], v[216:219], v[44:47]
	v_mfma_f32_16x16x32_bf16 v[40:43], v[184:187], v[216:219], v[40:43]
	v_mfma_f32_16x16x32_bf16 v[28:31], v[176:179], v[224:227], v[28:31]
	v_mfma_f32_16x16x32_bf16 v[24:27], v[184:187], v[224:227], v[24:27]
	v_mfma_f32_16x16x32_bf16 v[12:15], v[176:179], v[232:235], v[12:15]
	v_mfma_f32_16x16x32_bf16 v[8:11], v[184:187], v[232:235], v[8:11]
	v_mfma_f32_16x16x32_bf16 v[52:55], v[188:191], v[204:207], v[52:55]
	v_mfma_f32_16x16x32_bf16 v[48:51], v[196:199], v[204:207], v[48:51]
	v_mfma_f32_16x16x32_bf16 v[36:39], v[188:191], v[212:215], v[36:39]
	v_mfma_f32_16x16x32_bf16 v[32:35], v[196:199], v[212:215], v[32:35]
	v_mfma_f32_16x16x32_bf16 v[20:23], v[188:191], v[220:223], v[20:23]
	v_mfma_f32_16x16x32_bf16 v[16:19], v[196:199], v[220:223], v[16:19]
	v_mfma_f32_16x16x32_bf16 v[4:7], v[188:191], v[228:231], v[4:7]
	v_mfma_f32_16x16x32_bf16 v[0:3], v[196:199], v[228:231], v[0:3]
	v_mfma_f32_16x16x32_bf16 v[52:55], v[192:195], v[208:211], v[52:55]
	v_mfma_f32_16x16x32_bf16 v[48:51], v[200:203], v[208:211], v[48:51]
	v_mfma_f32_16x16x32_bf16 v[36:39], v[192:195], v[216:219], v[36:39]
	v_mfma_f32_16x16x32_bf16 v[32:35], v[200:203], v[216:219], v[32:35]
	v_mfma_f32_16x16x32_bf16 v[20:23], v[192:195], v[224:227], v[20:23]
	v_mfma_f32_16x16x32_bf16 v[16:19], v[200:203], v[224:227], v[16:19]
	v_mfma_f32_16x16x32_bf16 v[4:7], v[192:195], v[232:235], v[4:7]
	v_mfma_f32_16x16x32_bf16 v[0:3], v[200:203], v[232:235], v[0:3]
	s_setprio 0
	s_barrier
	s_add_i32 s28, 0, 0x18000
	ds_read_b128 v[172:175], v252 offset:32768
	ds_read_b128 v[176:179], v253 offset:32768
	s_add_i32 s29, 0, 0x1c000
	ds_read_b128 v[180:183], v252 offset:34816
	ds_read_b128 v[184:187], v253 offset:34816
	ds_read_b128 v[188:191], v252 offset:49152
	ds_read_b128 v[192:195], v253 offset:49152
	ds_read_b128 v[196:199], v252 offset:51200
	ds_read_b128 v[200:203], v253 offset:51200
	s_mov_b32 m0, s39
	v_lshl_add_u64 v[160:161], s[26:27], 0, v[160:161]
	ds_read_b128 v[204:207], v169 offset:32768
	ds_read_b128 v[208:211], v169 offset:33792
	ds_read_b128 v[212:215], v169 offset:34816
	ds_read_b128 v[216:219], v169 offset:35840
	ds_read_b128 v[220:223], v169 offset:36864
	ds_read_b128 v[224:227], v169 offset:37888
	ds_read_b128 v[228:231], v169 offset:38912
	ds_read_b128 v[232:235], v169 offset:39936
	global_load_lds_dwordx4 v[160:161], off
	v_lshl_add_u64 v[158:159], s[26:27], 0, v[158:159]
	s_mov_b32 m0, s40
	s_nop 0
	global_load_lds_dwordx4 v[158:159], off
	s_waitcnt vmcnt(8)
	s_waitcnt lgkmcnt(0)
	s_setprio 1
	s_barrier
	v_mfma_f32_16x16x32_bf16 v[140:143], v[172:175], v[204:207], v[140:143]
	v_mfma_f32_16x16x32_bf16 v[136:139], v[180:183], v[204:207], v[136:139]
	v_mfma_f32_16x16x32_bf16 v[124:127], v[172:175], v[212:215], v[124:127]
	v_mfma_f32_16x16x32_bf16 v[120:123], v[180:183], v[212:215], v[120:123]
	v_mfma_f32_16x16x32_bf16 v[92:95], v[172:175], v[220:223], v[92:95]
	v_mfma_f32_16x16x32_bf16 v[88:91], v[180:183], v[220:223], v[88:91]
	v_mfma_f32_16x16x32_bf16 v[76:79], v[172:175], v[228:231], v[76:79]
	v_mfma_f32_16x16x32_bf16 v[72:75], v[180:183], v[228:231], v[72:75]
	v_mfma_f32_16x16x32_bf16 v[140:143], v[176:179], v[208:211], v[140:143]
	v_mfma_f32_16x16x32_bf16 v[136:139], v[184:187], v[208:211], v[136:139]
	v_mfma_f32_16x16x32_bf16 v[124:127], v[176:179], v[216:219], v[124:127]
	v_mfma_f32_16x16x32_bf16 v[120:123], v[184:187], v[216:219], v[120:123]
	v_mfma_f32_16x16x32_bf16 v[92:95], v[176:179], v[224:227], v[92:95]
	v_mfma_f32_16x16x32_bf16 v[88:91], v[184:187], v[224:227], v[88:91]
	v_mfma_f32_16x16x32_bf16 v[76:79], v[176:179], v[232:235], v[76:79]
	v_mfma_f32_16x16x32_bf16 v[72:75], v[184:187], v[232:235], v[72:75]
	v_mfma_f32_16x16x32_bf16 v[132:135], v[188:191], v[204:207], v[132:135]
	v_mfma_f32_16x16x32_bf16 v[128:131], v[196:199], v[204:207], v[128:131]
	v_mfma_f32_16x16x32_bf16 v[108:111], v[188:191], v[212:215], v[108:111]
	v_mfma_f32_16x16x32_bf16 v[96:99], v[196:199], v[212:215], v[96:99]
	v_mfma_f32_16x16x32_bf16 v[84:87], v[188:191], v[220:223], v[84:87]
	v_mfma_f32_16x16x32_bf16 v[80:83], v[196:199], v[220:223], v[80:83]
	v_mfma_f32_16x16x32_bf16 v[68:71], v[188:191], v[228:231], v[68:71]
	v_mfma_f32_16x16x32_bf16 v[64:67], v[196:199], v[228:231], v[64:67]
	v_mfma_f32_16x16x32_bf16 v[132:135], v[192:195], v[208:211], v[132:135]
	v_mfma_f32_16x16x32_bf16 v[128:131], v[200:203], v[208:211], v[128:131]
	v_mfma_f32_16x16x32_bf16 v[108:111], v[192:195], v[216:219], v[108:111]
	v_mfma_f32_16x16x32_bf16 v[96:99], v[200:203], v[216:219], v[96:99]
	v_mfma_f32_16x16x32_bf16 v[84:87], v[192:195], v[224:227], v[84:87]
	v_mfma_f32_16x16x32_bf16 v[80:83], v[200:203], v[224:227], v[80:83]
	v_mfma_f32_16x16x32_bf16 v[68:71], v[192:195], v[232:235], v[68:71]
	v_mfma_f32_16x16x32_bf16 v[64:67], v[200:203], v[232:235], v[64:67]
	s_setprio 0
	s_barrier
	s_add_i32 s26, s28, s35
	v_lshl_add_u64 v[232:233], v[236:237], 0, s[14:15]
	s_mov_b32 m0, s26
	ds_read_b128 v[158:161], v169 offset:49152
	ds_read_b128 v[204:207], v169 offset:50176
	ds_read_b128 v[208:211], v169 offset:51200
	ds_read_b128 v[212:215], v169 offset:52224
	ds_read_b128 v[216:219], v169 offset:53248
	ds_read_b128 v[220:223], v169 offset:54272
	ds_read_b128 v[224:227], v169 offset:55296
	ds_read_b128 v[228:231], v169 offset:56320
	global_load_lds_dwordx4 v[232:233], off
	v_lshl_add_u64 v[232:233], v[238:239], 0, s[14:15]
	s_add_i32 m0, s26, 0x2000
	s_add_i32 s26, s29, s35
	global_load_lds_dwordx4 v[232:233], off
	v_lshl_add_u64 v[232:233], v[240:241], 0, s[14:15]
	s_mov_b32 m0, s26
	s_nop 0
	global_load_lds_dwordx4 v[232:233], off
	v_lshl_add_u64 v[232:233], v[242:243], 0, s[14:15]
	s_add_i32 m0, s26, 0x2000
	s_nop 0
	global_load_lds_dwordx4 v[232:233], off
	v_lshl_add_u64 v[232:233], v[244:245], 0, s[14:15]
	s_mov_b32 m0, s45
	s_nop 0
	global_load_lds_dwordx4 v[232:233], off
	v_lshl_add_u64 v[232:233], v[246:247], 0, s[14:15]
	s_mov_b32 m0, s46
	s_nop 0
	global_load_lds_dwordx4 v[232:233], off
	s_waitcnt vmcnt(8)
	s_waitcnt lgkmcnt(0)
	s_setprio 1
	s_barrier
	v_mfma_f32_16x16x32_bf16 v[60:63], v[172:175], v[158:161], v[60:63]
	v_mfma_f32_16x16x32_bf16 v[56:59], v[180:183], v[158:161], v[56:59]
	v_mfma_f32_16x16x32_bf16 v[44:47], v[172:175], v[208:211], v[44:47]
	v_mfma_f32_16x16x32_bf16 v[40:43], v[180:183], v[208:211], v[40:43]
	v_mfma_f32_16x16x32_bf16 v[28:31], v[172:175], v[216:219], v[28:31]
	v_mfma_f32_16x16x32_bf16 v[24:27], v[180:183], v[216:219], v[24:27]
	v_mfma_f32_16x16x32_bf16 v[12:15], v[172:175], v[224:227], v[12:15]
	v_mfma_f32_16x16x32_bf16 v[8:11], v[180:183], v[224:227], v[8:11]
	v_mfma_f32_16x16x32_bf16 v[60:63], v[176:179], v[204:207], v[60:63]
	v_mfma_f32_16x16x32_bf16 v[56:59], v[184:187], v[204:207], v[56:59]
	v_mfma_f32_16x16x32_bf16 v[44:47], v[176:179], v[212:215], v[44:47]
	v_mfma_f32_16x16x32_bf16 v[40:43], v[184:187], v[212:215], v[40:43]
	v_mfma_f32_16x16x32_bf16 v[28:31], v[176:179], v[220:223], v[28:31]
	v_mfma_f32_16x16x32_bf16 v[24:27], v[184:187], v[220:223], v[24:27]
	v_mfma_f32_16x16x32_bf16 v[12:15], v[176:179], v[228:231], v[12:15]
	v_mfma_f32_16x16x32_bf16 v[8:11], v[184:187], v[228:231], v[8:11]
	v_mfma_f32_16x16x32_bf16 v[52:55], v[188:191], v[158:161], v[52:55]
	v_mfma_f32_16x16x32_bf16 v[48:51], v[196:199], v[158:161], v[48:51]
	v_mfma_f32_16x16x32_bf16 v[36:39], v[188:191], v[208:211], v[36:39]
	v_mfma_f32_16x16x32_bf16 v[32:35], v[196:199], v[208:211], v[32:35]
	v_mfma_f32_16x16x32_bf16 v[20:23], v[188:191], v[216:219], v[20:23]
	v_mfma_f32_16x16x32_bf16 v[16:19], v[196:199], v[216:219], v[16:19]
	v_mfma_f32_16x16x32_bf16 v[4:7], v[188:191], v[224:227], v[4:7]
	v_mfma_f32_16x16x32_bf16 v[0:3], v[196:199], v[224:227], v[0:3]
	v_mfma_f32_16x16x32_bf16 v[52:55], v[192:195], v[204:207], v[52:55]
	v_mfma_f32_16x16x32_bf16 v[48:51], v[200:203], v[204:207], v[48:51]
	v_mfma_f32_16x16x32_bf16 v[36:39], v[192:195], v[212:215], v[36:39]
	v_mfma_f32_16x16x32_bf16 v[32:35], v[200:203], v[212:215], v[32:35]
	v_mfma_f32_16x16x32_bf16 v[20:23], v[192:195], v[220:223], v[20:23]
	v_mfma_f32_16x16x32_bf16 v[16:19], v[200:203], v[220:223], v[16:19]
	v_mfma_f32_16x16x32_bf16 v[4:7], v[192:195], v[228:231], v[4:7]
	v_mfma_f32_16x16x32_bf16 v[0:3], v[200:203], v[228:231], v[0:3]
	s_setprio 0
	s_barrier
	s_add_i32 s64, s64, 2
	s_add_u32 s24, s24, 0x100
	s_addc_u32 s25, s25, 0
	s_cmp_gt_u32 s64, 9
	s_cbranch_scc1 .LBB0_433

.LBB0_590:
	s_add_u32 s36, s8, s4
	s_addc_u32 s37, s9, s5
	s_add_u32 s38, s36, 0xe000100
	s_addc_u32 s39, s37, 0
	ds_read_b128 v[24:27], v252
	ds_read_b128 v[28:31], v253
	s_and_b64 s[36:37], s[40:41], exec
	ds_read_b128 v[16:19], v252 offset:2048
	ds_read_b128 v[20:23], v253 offset:2048
	s_cselect_b32 s37, s11, s39
	s_cselect_b32 s36, s10, s38
	s_add_u32 s90, s27, s4
	ds_read_b128 v[8:11], v252 offset:16384
	ds_read_b128 v[12:15], v253 offset:16384
	s_addc_u32 s91, s86, s5
	ds_read_b128 v[0:3], v252 offset:18432
	ds_read_b128 v[4:7], v253 offset:18432
	s_and_b64 s[38:39], s[40:41], exec
	s_cselect_b32 s39, s29, s91
	s_cselect_b32 s38, s28, s90
	s_add_u32 s90, s87, s4
	s_addc_u32 s91, s88, s5
	s_and_b64 s[40:41], s[40:41], exec
	s_cselect_b32 s41, s31, s91
	s_cselect_b32 s40, s30, s90
	s_add_u32 s100, s18, s4
	s_addc_u32 s101, s19, s5
	s_add_i32 m0, s61, 0xc000
	ds_read_b128 v[182:185], v201
	ds_read_b128 v[210:213], v201 offset:2048
	ds_read_b128 v[186:189], v202
	ds_read_b128 v[214:217], v202 offset:2048
	ds_read_b128 v[218:221], v201 offset:4096
	ds_read_b128 v[226:229], v201 offset:6144
	ds_read_b128 v[222:225], v202 offset:4096
	ds_read_b128 v[230:233], v202 offset:6144
	global_load_lds_dwordx4 v170, s[100:101]
	s_add_i32 m0, s61, 0xe000
	s_nop 0
	global_load_lds_dwordx4 v168, s[100:101]
	s_waitcnt vmcnt(8)
	s_waitcnt lgkmcnt(0)
	s_setprio 1
	s_barrier
	s_cmp_eq_u32 s4, 0
	s_cbranch_scc1 .Lc0_P6_0
	v_mfma_f32_16x16x128_f8f6f4 v[156:159], v[24:31], v[182:189], v[156:159]
	v_mfma_f32_16x16x128_f8f6f4 v[148:151], v[16:23], v[182:189], v[148:151]
	v_mfma_f32_16x16x128_f8f6f4 v[132:135], v[16:23], v[210:217], v[132:135]
	v_mfma_f32_16x16x128_f8f6f4 v[140:143], v[24:31], v[210:217], v[140:143]
	v_mfma_f32_16x16x128_f8f6f4 v[124:127], v[24:31], v[218:225], v[124:127]
	v_mfma_f32_16x16x128_f8f6f4 v[116:119], v[16:23], v[218:225], v[116:119]
	v_mfma_f32_16x16x128_f8f6f4 v[100:103], v[16:23], v[226:233], v[100:103]
	v_mfma_f32_16x16x128_f8f6f4 v[108:111], v[24:31], v[226:233], v[108:111]
	v_mfma_f32_16x16x128_f8f6f4 v[152:155], v[8:15], v[182:189], v[152:155]
	v_mfma_f32_16x16x128_f8f6f4 v[144:147], v[0:7], v[182:189], v[144:147]
	v_mfma_f32_16x16x128_f8f6f4 v[128:131], v[0:7], v[210:217], v[128:131]
	v_mfma_f32_16x16x128_f8f6f4 v[136:139], v[8:15], v[210:217], v[136:139]
	v_mfma_f32_16x16x128_f8f6f4 v[120:123], v[8:15], v[218:225], v[120:123]
	v_mfma_f32_16x16x128_f8f6f4 v[112:115], v[0:7], v[218:225], v[112:115]
	v_mfma_f32_16x16x128_f8f6f4 v[96:99], v[0:7], v[226:233], v[96:99]
	v_mfma_f32_16x16x128_f8f6f4 v[104:107], v[8:15], v[226:233], v[104:107]
.Lc0b_P6_0:
	s_setprio 0
	s_barrier
	s_add_i32 s90, s72, s44
	s_mov_b32 m0, s90
	ds_read_b128 v[210:213], v201 offset:16384
	ds_read_b128 v[218:221], v201 offset:18432
	ds_read_b128 v[214:217], v202 offset:16384
	ds_read_b128 v[222:225], v202 offset:18432
	ds_read_b128 v[226:229], v201 offset:20480
	ds_read_b128 v[234:237], v201 offset:22528
	ds_read_b128 v[230:233], v202 offset:20480
	ds_read_b128 v[238:241], v202 offset:22528
	global_load_lds_dwordx4 v160, s[38:39]
	s_add_i32 m0, s90, 0x2000
	s_add_i32 s98, s74, s44
	global_load_lds_dwordx4 v162, s[38:39]
	s_mov_b32 m0, s98
	s_nop 0
	global_load_lds_dwordx4 v160, s[40:41]
	s_add_i32 m0, s98, 0x2000
	v_mov_b32_e32 v167, v165
	global_load_lds_dwordx4 v162, s[40:41]
	s_waitcnt vmcnt(6)
	s_waitcnt lgkmcnt(0)
	s_setprio 1
	s_barrier
	s_cmp_eq_u32 s4, 0
	s_cbranch_scc1 .Lc0_P6_1
	v_mfma_f32_16x16x128_f8f6f4 v[92:95], v[24:31], v[210:217], v[92:95]
	v_mfma_f32_16x16x128_f8f6f4 v[84:87], v[16:23], v[210:217], v[84:87]
	v_mfma_f32_16x16x128_f8f6f4 v[68:71], v[16:23], v[218:225], v[68:71]
	v_mfma_f32_16x16x128_f8f6f4 v[76:79], v[24:31], v[218:225], v[76:79]
	s_mov_b32 m0, s61
	v_mfma_f32_16x16x128_f8f6f4 v[60:63], v[24:31], v[226:233], v[60:63]
	global_load_lds_dwordx4 v164, s[36:37]
	v_mfma_f32_16x16x128_f8f6f4 v[52:55], v[16:23], v[226:233], v[52:55]
	v_mfma_f32_16x16x128_f8f6f4 v[36:39], v[16:23], v[234:241], v[36:39]
	v_mfma_f32_16x16x128_f8f6f4 v[44:47], v[24:31], v[234:241], v[44:47]
	v_mfma_f32_16x16x128_f8f6f4 v[88:91], v[8:15], v[210:217], v[88:91]
	s_mov_b32 m0, s62
	v_mfma_f32_16x16x128_f8f6f4 v[80:83], v[0:7], v[210:217], v[80:83]
	global_load_lds_dwordx4 v166, s[36:37]
	v_mfma_f32_16x16x128_f8f6f4 v[64:67], v[0:7], v[218:225], v[64:67]
	v_mfma_f32_16x16x128_f8f6f4 v[72:75], v[8:15], v[218:225], v[72:75]
	v_mfma_f32_16x16x128_f8f6f4 v[56:59], v[8:15], v[226:233], v[56:59]
	v_mfma_f32_16x16x128_f8f6f4 v[48:51], v[0:7], v[226:233], v[48:51]
	v_mfma_f32_16x16x128_f8f6f4 v[32:35], v[0:7], v[234:241], v[32:35]
	v_mfma_f32_16x16x128_f8f6f4 v[40:43], v[8:15], v[234:241], v[40:43]
.Lc0b_P6_1:
	s_setprio 0
	s_barrier
	ds_read_b128 v[0:3], v252 offset:32768
	ds_read_b128 v[4:7], v253 offset:32768
	ds_read_b128 v[8:11], v252 offset:34816
	ds_read_b128 v[12:15], v253 offset:34816
	ds_read_b128 v[16:19], v252 offset:49152
	ds_read_b128 v[20:23], v253 offset:49152
	ds_read_b128 v[24:27], v252 offset:51200
	ds_read_b128 v[28:31], v253 offset:51200
	s_mov_b32 m0, s63
	ds_read_b128 v[210:213], v201 offset:32768
	ds_read_b128 v[218:221], v201 offset:34816
	ds_read_b128 v[214:217], v202 offset:32768
	ds_read_b128 v[222:225], v202 offset:34816
	ds_read_b128 v[226:229], v201 offset:36864
	ds_read_b128 v[234:237], v201 offset:38912
	ds_read_b128 v[230:233], v202 offset:36864
	ds_read_b128 v[238:241], v202 offset:38912
	global_load_lds_dwordx4 v180, s[36:37]
	s_mov_b32 m0, s64
	s_nop 0
	global_load_lds_dwordx4 v178, s[36:37]
	s_waitcnt vmcnt(8)
	s_waitcnt lgkmcnt(0)
	s_setprio 1
	s_barrier
	v_mfma_f32_16x16x128_f8f6f4 v[156:159], v[0:7], v[210:217], v[156:159]
	v_mfma_f32_16x16x128_f8f6f4 v[148:151], v[8:15], v[210:217], v[148:151]
	v_mfma_f32_16x16x128_f8f6f4 v[132:135], v[8:15], v[218:225], v[132:135]
	v_mfma_f32_16x16x128_f8f6f4 v[140:143], v[0:7], v[218:225], v[140:143]
	v_mfma_f32_16x16x128_f8f6f4 v[124:127], v[0:7], v[226:233], v[124:127]
	v_mfma_f32_16x16x128_f8f6f4 v[116:119], v[8:15], v[226:233], v[116:119]
	v_mfma_f32_16x16x128_f8f6f4 v[100:103], v[8:15], v[234:241], v[100:103]
	v_mfma_f32_16x16x128_f8f6f4 v[108:111], v[0:7], v[234:241], v[108:111]
	v_mfma_f32_16x16x128_f8f6f4 v[152:155], v[16:23], v[210:217], v[152:155]
	v_mfma_f32_16x16x128_f8f6f4 v[144:147], v[24:31], v[210:217], v[144:147]
	v_mfma_f32_16x16x128_f8f6f4 v[128:131], v[24:31], v[218:225], v[128:131]
	v_mfma_f32_16x16x128_f8f6f4 v[136:139], v[16:23], v[218:225], v[136:139]
	v_mfma_f32_16x16x128_f8f6f4 v[120:123], v[16:23], v[226:233], v[120:123]
	v_mfma_f32_16x16x128_f8f6f4 v[112:115], v[24:31], v[226:233], v[112:115]
	v_mfma_f32_16x16x128_f8f6f4 v[96:99], v[24:31], v[234:241], v[96:99]
	v_mfma_f32_16x16x128_f8f6f4 v[104:107], v[16:23], v[234:241], v[104:107]
	s_setprio 0
	s_barrier
	s_add_i32 s99, s44, 0x17f80
	s_mov_b32 m0, s99
	ds_read_b128 v[210:213], v201 offset:49152
	ds_read_b128 v[218:221], v201 offset:51200
	ds_read_b128 v[214:217], v202 offset:49152
	ds_read_b128 v[222:225], v202 offset:51200
	ds_read_b128 v[226:229], v201 offset:53248
	ds_read_b128 v[234:237], v201 offset:55296
	ds_read_b128 v[230:233], v202 offset:53248
	ds_read_b128 v[238:241], v202 offset:55296
	global_load_lds_dwordx4 v160, s[38:39] offset:128
	s_add_i32 m0, s99, 0x2000
	s_add_i32 s99, s44, 0x1bf80
	global_load_lds_dwordx4 v162, s[38:39] offset:128
	s_mov_b32 m0, s99
	s_nop 0
	global_load_lds_dwordx4 v160, s[40:41] offset:128
	s_add_i32 m0, s99, 0x2000
	s_nop 0
	global_load_lds_dwordx4 v162, s[40:41] offset:128
	s_waitcnt vmcnt(6)
	s_waitcnt lgkmcnt(0)
	s_setprio 1
	s_barrier
	v_mfma_f32_16x16x128_f8f6f4 v[92:95], v[0:7], v[210:217], v[92:95]
	v_mfma_f32_16x16x128_f8f6f4 v[84:87], v[8:15], v[210:217], v[84:87]
	v_mfma_f32_16x16x128_f8f6f4 v[68:71], v[8:15], v[218:225], v[68:71]
	v_mfma_f32_16x16x128_f8f6f4 v[76:79], v[0:7], v[218:225], v[76:79]
	s_add_i32 m0, s65, 0xffffff80
	v_mfma_f32_16x16x128_f8f6f4 v[60:63], v[0:7], v[226:233], v[60:63]
	global_load_lds_dwordx4 v164, s[36:37] offset:128
	v_mfma_f32_16x16x128_f8f6f4 v[52:55], v[8:15], v[226:233], v[52:55]
	v_mfma_f32_16x16x128_f8f6f4 v[36:39], v[8:15], v[234:241], v[36:39]
	v_mfma_f32_16x16x128_f8f6f4 v[44:47], v[0:7], v[234:241], v[44:47]
	v_mfma_f32_16x16x128_f8f6f4 v[88:91], v[16:23], v[210:217], v[88:91]
	s_add_i32 m0, s66, 0xffffff80
	v_mfma_f32_16x16x128_f8f6f4 v[80:83], v[24:31], v[210:217], v[80:83]
	global_load_lds_dwordx4 v166, s[36:37] offset:128
	v_mfma_f32_16x16x128_f8f6f4 v[64:67], v[24:31], v[218:225], v[64:67]
	v_mfma_f32_16x16x128_f8f6f4 v[72:75], v[16:23], v[218:225], v[72:75]
	v_mfma_f32_16x16x128_f8f6f4 v[56:59], v[16:23], v[226:233], v[56:59]
	v_mfma_f32_16x16x128_f8f6f4 v[48:51], v[24:31], v[226:233], v[48:51]
	v_mfma_f32_16x16x128_f8f6f4 v[32:35], v[24:31], v[234:241], v[32:35]
	v_mfma_f32_16x16x128_f8f6f4 v[40:43], v[16:23], v[234:241], v[40:43]
	s_setprio 0
	s_barrier
	s_add_i32 s89, s89, 2
	s_add_u32 s4, s4, 0x100
	s_addc_u32 s5, s5, 0
	s_cmp_gt_u32 s89, 5
	s_cbranch_scc1 .LBB0_593

.LBB0_672:
	s_add_u32 s36, s6, s34
	s_addc_u32 s37, s7, s35
	s_add_u32 s38, s36, 0x12c00100
	s_addc_u32 s39, s37, 0
	ds_read_b128 v[24:27], v252
	ds_read_b128 v[28:31], v253
	s_and_b64 s[36:37], s[40:41], exec
	ds_read_b128 v[16:19], v252 offset:2048
	ds_read_b128 v[20:23], v253 offset:2048
	s_cselect_b32 s37, s9, s39
	s_cselect_b32 s36, s8, s38
	s_add_u32 s86, s27, s34
	ds_read_b128 v[8:11], v252 offset:16384
	ds_read_b128 v[12:15], v253 offset:16384
	s_addc_u32 s87, s82, s35
	ds_read_b128 v[0:3], v252 offset:18432
	ds_read_b128 v[4:7], v253 offset:18432
	s_and_b64 s[38:39], s[40:41], exec
	s_cselect_b32 s39, s29, s87
	s_cselect_b32 s38, s28, s86
	s_add_u32 s86, s83, s34
	s_addc_u32 s87, s84, s35
	s_and_b64 s[40:41], s[40:41], exec
	s_cselect_b32 s41, s31, s87
	s_cselect_b32 s40, s30, s86
	s_add_u32 s100, s16, s34
	s_addc_u32 s101, s17, s35
	s_add_i32 m0, s59, 0xc000
	ds_read_b128 v[186:189], v207
	ds_read_b128 v[216:219], v207 offset:2048
	ds_read_b128 v[190:193], v208
	ds_read_b128 v[220:223], v208 offset:2048
	ds_read_b128 v[224:227], v207 offset:4096
	ds_read_b128 v[232:235], v207 offset:6144
	ds_read_b128 v[228:231], v208 offset:4096
	ds_read_b128 v[236:239], v208 offset:6144
	global_load_lds_dwordx4 v166, s[100:101]
	s_add_i32 m0, s59, 0xe000
	s_nop 0
	global_load_lds_dwordx4 v168, s[100:101]
	s_waitcnt vmcnt(8)
	s_waitcnt lgkmcnt(0)
	s_setprio 1
	s_barrier
	s_cmp_eq_u32 s34, 0
	s_cbranch_scc1 .Lc0_P7_0
	v_mfma_f32_16x16x128_f8f6f4 v[156:159], v[24:31], v[186:193], v[156:159]
	v_mfma_f32_16x16x128_f8f6f4 v[152:155], v[16:23], v[186:193], v[152:155]
	v_mfma_f32_16x16x128_f8f6f4 v[136:139], v[16:23], v[216:223], v[136:139]
	v_mfma_f32_16x16x128_f8f6f4 v[140:143], v[24:31], v[216:223], v[140:143]
	v_mfma_f32_16x16x128_f8f6f4 v[124:127], v[24:31], v[224:231], v[124:127]
	v_mfma_f32_16x16x128_f8f6f4 v[120:123], v[16:23], v[224:231], v[120:123]
	v_mfma_f32_16x16x128_f8f6f4 v[104:107], v[16:23], v[232:239], v[104:107]
	v_mfma_f32_16x16x128_f8f6f4 v[108:111], v[24:31], v[232:239], v[108:111]
	v_mfma_f32_16x16x128_f8f6f4 v[148:151], v[8:15], v[186:193], v[148:151]
	v_mfma_f32_16x16x128_f8f6f4 v[144:147], v[0:7], v[186:193], v[144:147]
	v_mfma_f32_16x16x128_f8f6f4 v[128:131], v[0:7], v[216:223], v[128:131]
	v_mfma_f32_16x16x128_f8f6f4 v[132:135], v[8:15], v[216:223], v[132:135]
	v_mfma_f32_16x16x128_f8f6f4 v[116:119], v[8:15], v[224:231], v[116:119]
	v_mfma_f32_16x16x128_f8f6f4 v[112:115], v[0:7], v[224:231], v[112:115]
	v_mfma_f32_16x16x128_f8f6f4 v[96:99], v[0:7], v[232:239], v[96:99]
	v_mfma_f32_16x16x128_f8f6f4 v[100:103], v[8:15], v[232:239], v[100:103]
.Lc0b_P7_0:
	s_setprio 0
	s_barrier
	s_add_i32 s86, s69, s42
	s_mov_b32 m0, s86
	ds_read_b128 v[216:219], v207 offset:16384
	ds_read_b128 v[224:227], v207 offset:18432
	ds_read_b128 v[220:223], v208 offset:16384
	ds_read_b128 v[228:231], v208 offset:18432
	ds_read_b128 v[232:235], v207 offset:20480
	ds_read_b128 v[240:243], v207 offset:22528
	ds_read_b128 v[236:239], v208 offset:20480
	ds_read_b128 v[244:247], v208 offset:22528
	global_load_lds_dwordx4 v160, s[38:39]
	s_add_i32 m0, s86, 0x2000
	s_add_i32 s98, s71, s42
	global_load_lds_dwordx4 v162, s[38:39]
	s_mov_b32 m0, s98
	s_nop 0
	global_load_lds_dwordx4 v160, s[40:41]
	s_add_i32 m0, s98, 0x2000
	v_mov_b32_e32 v173, v165
	global_load_lds_dwordx4 v162, s[40:41]
	s_waitcnt vmcnt(6)
	s_waitcnt lgkmcnt(0)
	s_setprio 1
	s_barrier
	s_cmp_eq_u32 s34, 0
	s_cbranch_scc1 .Lc0_P7_1
	v_mfma_f32_16x16x128_f8f6f4 v[92:95], v[24:31], v[216:223], v[92:95]
	v_mfma_f32_16x16x128_f8f6f4 v[88:91], v[16:23], v[216:223], v[88:91]
	v_mfma_f32_16x16x128_f8f6f4 v[72:75], v[16:23], v[224:231], v[72:75]
	v_mfma_f32_16x16x128_f8f6f4 v[76:79], v[24:31], v[224:231], v[76:79]
	s_mov_b32 m0, s59
	v_mfma_f32_16x16x128_f8f6f4 v[60:63], v[24:31], v[232:239], v[60:63]
	global_load_lds_dwordx4 v164, s[36:37]
	v_mfma_f32_16x16x128_f8f6f4 v[56:59], v[16:23], v[232:239], v[56:59]
	v_mfma_f32_16x16x128_f8f6f4 v[40:43], v[16:23], v[240:247], v[40:43]
	v_mfma_f32_16x16x128_f8f6f4 v[44:47], v[24:31], v[240:247], v[44:47]
	v_mfma_f32_16x16x128_f8f6f4 v[84:87], v[8:15], v[216:223], v[84:87]
	s_mov_b32 m0, s60
	v_mfma_f32_16x16x128_f8f6f4 v[80:83], v[0:7], v[216:223], v[80:83]
	global_load_lds_dwordx4 v172, s[36:37]
	v_mfma_f32_16x16x128_f8f6f4 v[64:67], v[0:7], v[224:231], v[64:67]
	v_mfma_f32_16x16x128_f8f6f4 v[68:71], v[8:15], v[224:231], v[68:71]
	v_mfma_f32_16x16x128_f8f6f4 v[52:55], v[8:15], v[232:239], v[52:55]
	v_mfma_f32_16x16x128_f8f6f4 v[48:51], v[0:7], v[232:239], v[48:51]
	v_mfma_f32_16x16x128_f8f6f4 v[32:35], v[0:7], v[240:247], v[32:35]
	v_mfma_f32_16x16x128_f8f6f4 v[36:39], v[8:15], v[240:247], v[36:39]
.Lc0b_P7_1:
	s_setprio 0
	s_barrier
	ds_read_b128 v[0:3], v252 offset:32768
	ds_read_b128 v[4:7], v253 offset:32768
	ds_read_b128 v[8:11], v252 offset:34816
	ds_read_b128 v[12:15], v253 offset:34816
	ds_read_b128 v[16:19], v252 offset:49152
	ds_read_b128 v[20:23], v253 offset:49152
	ds_read_b128 v[24:27], v252 offset:51200
	ds_read_b128 v[28:31], v253 offset:51200
	s_mov_b32 m0, s61
	ds_read_b128 v[216:219], v207 offset:32768
	ds_read_b128 v[224:227], v207 offset:34816
	ds_read_b128 v[220:223], v208 offset:32768
	ds_read_b128 v[228:231], v208 offset:34816
	ds_read_b128 v[232:235], v207 offset:36864
	ds_read_b128 v[240:243], v207 offset:38912
	ds_read_b128 v[236:239], v208 offset:36864
	ds_read_b128 v[244:247], v208 offset:38912
	global_load_lds_dwordx4 v184, s[36:37]
	s_mov_b32 m0, s62
	s_nop 0
	global_load_lds_dwordx4 v182, s[36:37]
	s_waitcnt vmcnt(8)
	s_waitcnt lgkmcnt(0)
	s_setprio 1
	s_barrier
	v_mfma_f32_16x16x128_f8f6f4 v[156:159], v[0:7], v[216:223], v[156:159]
	v_mfma_f32_16x16x128_f8f6f4 v[152:155], v[8:15], v[216:223], v[152:155]
	v_mfma_f32_16x16x128_f8f6f4 v[136:139], v[8:15], v[224:231], v[136:139]
	v_mfma_f32_16x16x128_f8f6f4 v[140:143], v[0:7], v[224:231], v[140:143]
	v_mfma_f32_16x16x128_f8f6f4 v[124:127], v[0:7], v[232:239], v[124:127]
	v_mfma_f32_16x16x128_f8f6f4 v[120:123], v[8:15], v[232:239], v[120:123]
	v_mfma_f32_16x16x128_f8f6f4 v[104:107], v[8:15], v[240:247], v[104:107]
	v_mfma_f32_16x16x128_f8f6f4 v[108:111], v[0:7], v[240:247], v[108:111]
	v_mfma_f32_16x16x128_f8f6f4 v[148:151], v[16:23], v[216:223], v[148:151]
	v_mfma_f32_16x16x128_f8f6f4 v[144:147], v[24:31], v[216:223], v[144:147]
	v_mfma_f32_16x16x128_f8f6f4 v[128:131], v[24:31], v[224:231], v[128:131]
	v_mfma_f32_16x16x128_f8f6f4 v[132:135], v[16:23], v[224:231], v[132:135]
	v_mfma_f32_16x16x128_f8f6f4 v[116:119], v[16:23], v[232:239], v[116:119]
	v_mfma_f32_16x16x128_f8f6f4 v[112:115], v[24:31], v[232:239], v[112:115]
	v_mfma_f32_16x16x128_f8f6f4 v[96:99], v[24:31], v[240:247], v[96:99]
	v_mfma_f32_16x16x128_f8f6f4 v[100:103], v[16:23], v[240:247], v[100:103]
	s_setprio 0
	s_barrier
	s_add_i32 s99, s42, 0x17f80
	s_mov_b32 m0, s99
	ds_read_b128 v[216:219], v207 offset:49152
	ds_read_b128 v[224:227], v207 offset:51200
	ds_read_b128 v[220:223], v208 offset:49152
	ds_read_b128 v[228:231], v208 offset:51200
	ds_read_b128 v[232:235], v207 offset:53248
	ds_read_b128 v[240:243], v207 offset:55296
	ds_read_b128 v[236:239], v208 offset:53248
	ds_read_b128 v[244:247], v208 offset:55296
	global_load_lds_dwordx4 v160, s[38:39] offset:128
	s_add_i32 m0, s99, 0x2000
	s_add_i32 s99, s42, 0x1bf80
	global_load_lds_dwordx4 v162, s[38:39] offset:128
	s_mov_b32 m0, s99
	s_nop 0
	global_load_lds_dwordx4 v160, s[40:41] offset:128
	s_add_i32 m0, s99, 0x2000
	s_nop 0
	global_load_lds_dwordx4 v162, s[40:41] offset:128
	s_waitcnt vmcnt(6)
	s_waitcnt lgkmcnt(0)
	s_setprio 1
	s_barrier
	v_mfma_f32_16x16x128_f8f6f4 v[92:95], v[0:7], v[216:223], v[92:95]
	v_mfma_f32_16x16x128_f8f6f4 v[88:91], v[8:15], v[216:223], v[88:91]
	v_mfma_f32_16x16x128_f8f6f4 v[72:75], v[8:15], v[224:231], v[72:75]
	v_mfma_f32_16x16x128_f8f6f4 v[76:79], v[0:7], v[224:231], v[76:79]
	s_add_i32 m0, s63, 0xffffff80
	v_mfma_f32_16x16x128_f8f6f4 v[60:63], v[0:7], v[232:239], v[60:63]
	global_load_lds_dwordx4 v164, s[36:37] offset:128
	v_mfma_f32_16x16x128_f8f6f4 v[56:59], v[8:15], v[232:239], v[56:59]
	v_mfma_f32_16x16x128_f8f6f4 v[40:43], v[8:15], v[240:247], v[40:43]
	v_mfma_f32_16x16x128_f8f6f4 v[44:47], v[0:7], v[240:247], v[44:47]
	v_mfma_f32_16x16x128_f8f6f4 v[84:87], v[16:23], v[216:223], v[84:87]
	s_add_i32 m0, s64, 0xffffff80
	v_mfma_f32_16x16x128_f8f6f4 v[80:83], v[24:31], v[216:223], v[80:83]
	global_load_lds_dwordx4 v172, s[36:37] offset:128
	v_mfma_f32_16x16x128_f8f6f4 v[64:67], v[24:31], v[224:231], v[64:67]
	v_mfma_f32_16x16x128_f8f6f4 v[68:71], v[16:23], v[224:231], v[68:71]
	v_mfma_f32_16x16x128_f8f6f4 v[52:55], v[16:23], v[232:239], v[52:55]
	v_mfma_f32_16x16x128_f8f6f4 v[48:51], v[24:31], v[232:239], v[48:51]
	v_mfma_f32_16x16x128_f8f6f4 v[32:35], v[24:31], v[240:247], v[32:35]
	v_mfma_f32_16x16x128_f8f6f4 v[36:39], v[16:23], v[240:247], v[36:39]
	s_setprio 0
	s_barrier
	s_add_i32 s85, s85, 2
	s_add_u32 s34, s34, 0x100
	s_addc_u32 s35, s35, 0
	s_cmp_gt_u32 s85, 5
	s_cbranch_scc1 .LBB0_675

.LBB0_817:
	s_add_u32 s28, s10, s26
	s_addc_u32 s29, s11, s27
	s_add_u32 s30, s28, 0x38000100
	s_addc_u32 s31, s29, 0
	ds_read_b128 v[24:27], v252
	ds_read_b128 v[28:31], v253
	s_and_b64 s[28:29], s[34:35], exec
	ds_read_b128 v[16:19], v252 offset:2048
	ds_read_b128 v[20:23], v253 offset:2048
	s_cselect_b32 s29, s1, s31
	s_cselect_b32 s28, s0, s30
	s_add_u32 s61, s56, s26
	ds_read_b128 v[8:11], v252 offset:16384
	ds_read_b128 v[12:15], v253 offset:16384
	s_addc_u32 s62, s57, s27
	ds_read_b128 v[0:3], v252 offset:18432
	ds_read_b128 v[4:7], v253 offset:18432
	s_and_b64 s[30:31], s[34:35], exec
	s_cselect_b32 s31, s23, s62
	s_cselect_b32 s30, s22, s61
	s_add_u32 s61, s58, s26
	s_addc_u32 s62, s59, s27
	s_and_b64 s[34:35], s[34:35], exec
	s_cselect_b32 s35, s25, s62
	s_cselect_b32 s34, s24, s61
	s_add_u32 s100, s14, s26
	s_addc_u32 s101, s15, s27
	s_add_i32 m0, s37, 0xc000
	ds_read_b128 v[186:189], v207
	ds_read_b128 v[216:219], v207 offset:2048
	ds_read_b128 v[190:193], v208
	ds_read_b128 v[220:223], v208 offset:2048
	ds_read_b128 v[224:227], v207 offset:4096
	ds_read_b128 v[232:235], v207 offset:6144
	ds_read_b128 v[228:231], v208 offset:4096
	ds_read_b128 v[236:239], v208 offset:6144
	global_load_lds_dwordx4 v168, s[100:101]
	s_add_i32 m0, s37, 0xe000
	s_nop 0
	global_load_lds_dwordx4 v170, s[100:101]
	s_waitcnt vmcnt(8)
	s_waitcnt lgkmcnt(0)
	s_setprio 1
	s_barrier
	s_cmp_eq_u32 s26, 0
	s_cbranch_scc1 .Lc0_P9a_0
	v_mfma_f32_16x16x128_f8f6f4 v[156:159], v[24:31], v[186:193], v[156:159]
	v_mfma_f32_16x16x128_f8f6f4 v[152:155], v[16:23], v[186:193], v[152:155]
	v_mfma_f32_16x16x128_f8f6f4 v[136:139], v[16:23], v[216:223], v[136:139]
	v_mfma_f32_16x16x128_f8f6f4 v[140:143], v[24:31], v[216:223], v[140:143]
	v_mfma_f32_16x16x128_f8f6f4 v[124:127], v[24:31], v[224:231], v[124:127]
	v_mfma_f32_16x16x128_f8f6f4 v[120:123], v[16:23], v[224:231], v[120:123]
	v_mfma_f32_16x16x128_f8f6f4 v[104:107], v[16:23], v[232:239], v[104:107]
	v_mfma_f32_16x16x128_f8f6f4 v[108:111], v[24:31], v[232:239], v[108:111]
	v_mfma_f32_16x16x128_f8f6f4 v[148:151], v[8:15], v[186:193], v[148:151]
	v_mfma_f32_16x16x128_f8f6f4 v[144:147], v[0:7], v[186:193], v[144:147]
	v_mfma_f32_16x16x128_f8f6f4 v[128:131], v[0:7], v[216:223], v[128:131]
	v_mfma_f32_16x16x128_f8f6f4 v[132:135], v[8:15], v[216:223], v[132:135]
	v_mfma_f32_16x16x128_f8f6f4 v[116:119], v[8:15], v[224:231], v[116:119]
	v_mfma_f32_16x16x128_f8f6f4 v[112:115], v[0:7], v[224:231], v[112:115]
	v_mfma_f32_16x16x128_f8f6f4 v[96:99], v[0:7], v[232:239], v[96:99]
	v_mfma_f32_16x16x128_f8f6f4 v[100:103], v[8:15], v[232:239], v[100:103]
.Lc0b_P9a_0:
	s_setprio 0
	s_barrier
	s_add_i32 s61, s44, s36
	s_mov_b32 m0, s61
	ds_read_b128 v[216:219], v207 offset:16384
	ds_read_b128 v[224:227], v207 offset:18432
	ds_read_b128 v[220:223], v208 offset:16384
	ds_read_b128 v[228:231], v208 offset:18432
	ds_read_b128 v[232:235], v207 offset:20480
	ds_read_b128 v[240:243], v207 offset:22528
	ds_read_b128 v[236:239], v208 offset:20480
	ds_read_b128 v[244:247], v208 offset:22528
	global_load_lds_dwordx4 v160, s[30:31]
	s_add_i32 m0, s61, 0x2000
	s_add_i32 s98, s46, s36
	global_load_lds_dwordx4 v162, s[30:31]
	s_mov_b32 m0, s98
	s_nop 0
	global_load_lds_dwordx4 v160, s[34:35]
	s_add_i32 m0, s98, 0x2000
	v_mov_b32_e32 v167, v165
	global_load_lds_dwordx4 v162, s[34:35]
	s_waitcnt vmcnt(6)
	s_waitcnt lgkmcnt(0)
	s_setprio 1
	s_barrier
	s_cmp_eq_u32 s26, 0
	s_cbranch_scc1 .Lc0_P9a_1
	v_mfma_f32_16x16x128_f8f6f4 v[92:95], v[24:31], v[216:223], v[92:95]
	v_mfma_f32_16x16x128_f8f6f4 v[88:91], v[16:23], v[216:223], v[88:91]
	v_mfma_f32_16x16x128_f8f6f4 v[72:75], v[16:23], v[224:231], v[72:75]
	v_mfma_f32_16x16x128_f8f6f4 v[76:79], v[24:31], v[224:231], v[76:79]
	s_mov_b32 m0, s37
	v_mfma_f32_16x16x128_f8f6f4 v[60:63], v[24:31], v[232:239], v[60:63]
	global_load_lds_dwordx4 v164, s[28:29]
	v_mfma_f32_16x16x128_f8f6f4 v[56:59], v[16:23], v[232:239], v[56:59]
	v_mfma_f32_16x16x128_f8f6f4 v[40:43], v[16:23], v[240:247], v[40:43]
	v_mfma_f32_16x16x128_f8f6f4 v[44:47], v[24:31], v[240:247], v[44:47]
	v_mfma_f32_16x16x128_f8f6f4 v[84:87], v[8:15], v[216:223], v[84:87]
	s_mov_b32 m0, s38
	v_mfma_f32_16x16x128_f8f6f4 v[80:83], v[0:7], v[216:223], v[80:83]
	global_load_lds_dwordx4 v166, s[28:29]
	v_mfma_f32_16x16x128_f8f6f4 v[64:67], v[0:7], v[224:231], v[64:67]
	v_mfma_f32_16x16x128_f8f6f4 v[68:71], v[8:15], v[224:231], v[68:71]
	v_mfma_f32_16x16x128_f8f6f4 v[52:55], v[8:15], v[232:239], v[52:55]
	v_mfma_f32_16x16x128_f8f6f4 v[48:51], v[0:7], v[232:239], v[48:51]
	v_mfma_f32_16x16x128_f8f6f4 v[32:35], v[0:7], v[240:247], v[32:35]
	v_mfma_f32_16x16x128_f8f6f4 v[36:39], v[8:15], v[240:247], v[36:39]
.Lc0b_P9a_1:
	s_setprio 0
	s_barrier
	ds_read_b128 v[0:3], v252 offset:32768
	ds_read_b128 v[4:7], v253 offset:32768
	ds_read_b128 v[8:11], v252 offset:34816
	ds_read_b128 v[12:15], v253 offset:34816
	ds_read_b128 v[16:19], v252 offset:49152
	ds_read_b128 v[20:23], v253 offset:49152
	ds_read_b128 v[24:27], v252 offset:51200
	ds_read_b128 v[28:31], v253 offset:51200
	s_mov_b32 m0, s39
	ds_read_b128 v[216:219], v207 offset:32768
	ds_read_b128 v[224:227], v207 offset:34816
	ds_read_b128 v[220:223], v208 offset:32768
	ds_read_b128 v[228:231], v208 offset:34816
	ds_read_b128 v[232:235], v207 offset:36864
	ds_read_b128 v[240:243], v207 offset:38912
	ds_read_b128 v[236:239], v208 offset:36864
	ds_read_b128 v[244:247], v208 offset:38912
	global_load_lds_dwordx4 v184, s[28:29]
	s_mov_b32 m0, s40
	s_nop 0
	global_load_lds_dwordx4 v182, s[28:29]
	s_waitcnt vmcnt(8)
	s_waitcnt lgkmcnt(0)
	s_setprio 1
	s_barrier
	v_mfma_f32_16x16x128_f8f6f4 v[156:159], v[0:7], v[216:223], v[156:159]
	v_mfma_f32_16x16x128_f8f6f4 v[152:155], v[8:15], v[216:223], v[152:155]
	v_mfma_f32_16x16x128_f8f6f4 v[136:139], v[8:15], v[224:231], v[136:139]
	v_mfma_f32_16x16x128_f8f6f4 v[140:143], v[0:7], v[224:231], v[140:143]
	v_mfma_f32_16x16x128_f8f6f4 v[124:127], v[0:7], v[232:239], v[124:127]
	v_mfma_f32_16x16x128_f8f6f4 v[120:123], v[8:15], v[232:239], v[120:123]
	v_mfma_f32_16x16x128_f8f6f4 v[104:107], v[8:15], v[240:247], v[104:107]
	v_mfma_f32_16x16x128_f8f6f4 v[108:111], v[0:7], v[240:247], v[108:111]
	v_mfma_f32_16x16x128_f8f6f4 v[148:151], v[16:23], v[216:223], v[148:151]
	v_mfma_f32_16x16x128_f8f6f4 v[144:147], v[24:31], v[216:223], v[144:147]
	v_mfma_f32_16x16x128_f8f6f4 v[128:131], v[24:31], v[224:231], v[128:131]
	v_mfma_f32_16x16x128_f8f6f4 v[132:135], v[16:23], v[224:231], v[132:135]
	v_mfma_f32_16x16x128_f8f6f4 v[116:119], v[16:23], v[232:239], v[116:119]
	v_mfma_f32_16x16x128_f8f6f4 v[112:115], v[24:31], v[232:239], v[112:115]
	v_mfma_f32_16x16x128_f8f6f4 v[96:99], v[24:31], v[240:247], v[96:99]
	v_mfma_f32_16x16x128_f8f6f4 v[100:103], v[16:23], v[240:247], v[100:103]
	s_setprio 0
	s_barrier
	s_add_i32 s99, s36, 0x17f80
	s_mov_b32 m0, s99
	ds_read_b128 v[216:219], v207 offset:49152
	ds_read_b128 v[224:227], v207 offset:51200
	ds_read_b128 v[220:223], v208 offset:49152
	ds_read_b128 v[228:231], v208 offset:51200
	ds_read_b128 v[232:235], v207 offset:53248
	ds_read_b128 v[240:243], v207 offset:55296
	ds_read_b128 v[236:239], v208 offset:53248
	ds_read_b128 v[244:247], v208 offset:55296
	global_load_lds_dwordx4 v160, s[30:31] offset:128
	s_add_i32 m0, s99, 0x2000
	s_add_i32 s99, s36, 0x1bf80
	global_load_lds_dwordx4 v162, s[30:31] offset:128
	s_mov_b32 m0, s99
	s_nop 0
	global_load_lds_dwordx4 v160, s[34:35] offset:128
	s_add_i32 m0, s99, 0x2000
	s_nop 0
	global_load_lds_dwordx4 v162, s[34:35] offset:128
	s_waitcnt vmcnt(6)
	s_waitcnt lgkmcnt(0)
	s_setprio 1
	s_barrier
	v_mfma_f32_16x16x128_f8f6f4 v[92:95], v[0:7], v[216:223], v[92:95]
	v_mfma_f32_16x16x128_f8f6f4 v[88:91], v[8:15], v[216:223], v[88:91]
	v_mfma_f32_16x16x128_f8f6f4 v[72:75], v[8:15], v[224:231], v[72:75]
	v_mfma_f32_16x16x128_f8f6f4 v[76:79], v[0:7], v[224:231], v[76:79]
	s_add_i32 m0, s41, 0xffffff80
	v_mfma_f32_16x16x128_f8f6f4 v[60:63], v[0:7], v[232:239], v[60:63]
	global_load_lds_dwordx4 v164, s[28:29] offset:128
	v_mfma_f32_16x16x128_f8f6f4 v[56:59], v[8:15], v[232:239], v[56:59]
	v_mfma_f32_16x16x128_f8f6f4 v[40:43], v[8:15], v[240:247], v[40:43]
	v_mfma_f32_16x16x128_f8f6f4 v[44:47], v[0:7], v[240:247], v[44:47]
	v_mfma_f32_16x16x128_f8f6f4 v[84:87], v[16:23], v[216:223], v[84:87]
	s_add_i32 m0, s42, 0xffffff80
	v_mfma_f32_16x16x128_f8f6f4 v[80:83], v[24:31], v[216:223], v[80:83]
	global_load_lds_dwordx4 v166, s[28:29] offset:128
	v_mfma_f32_16x16x128_f8f6f4 v[64:67], v[24:31], v[224:231], v[64:67]
	v_mfma_f32_16x16x128_f8f6f4 v[68:71], v[16:23], v[224:231], v[68:71]
	v_mfma_f32_16x16x128_f8f6f4 v[52:55], v[16:23], v[232:239], v[52:55]
	v_mfma_f32_16x16x128_f8f6f4 v[48:51], v[24:31], v[232:239], v[48:51]
	v_mfma_f32_16x16x128_f8f6f4 v[32:35], v[24:31], v[240:247], v[32:35]
	v_mfma_f32_16x16x128_f8f6f4 v[36:39], v[16:23], v[240:247], v[36:39]
	s_setprio 0
	s_barrier
	s_add_i32 s60, s60, 2
	s_add_u32 s26, s26, 0x100
	s_addc_u32 s27, s27, 0
	s_cmp_gt_u32 s60, 5
	s_cbranch_scc1 .LBB0_820

.LBB0_839:
	s_add_u32 s6, s10, s4
	s_addc_u32 s7, s11, s5
	s_add_u32 s34, s6, 0xe000100
	s_addc_u32 s35, s7, 0
	ds_read_b128 v[166:169], v252
	ds_read_b128 v[170:173], v253
	s_and_b64 s[6:7], s[30:31], exec
	ds_read_b128 v[174:177], v252 offset:2048
	ds_read_b128 v[178:181], v253 offset:2048
	s_cselect_b32 s7, s1, s35
	s_cselect_b32 s6, s0, s34
	s_add_u32 s62, s36, s4
	ds_read_b128 v[182:185], v252 offset:16384
	ds_read_b128 v[186:189], v253 offset:16384
	s_addc_u32 s63, s37, s5
	ds_read_b128 v[190:193], v252 offset:18432
	ds_read_b128 v[194:197], v253 offset:18432
	s_and_b64 s[34:35], s[30:31], exec
	s_cselect_b32 s35, s27, s63
	s_cselect_b32 s34, s26, s62
	s_add_u32 s62, s57, s4
	s_addc_u32 s63, s60, s5
	s_and_b64 s[30:31], s[30:31], exec
	s_cselect_b32 s31, s29, s63
	s_cselect_b32 s30, s28, s62
	v_lshl_add_u64 v[232:233], v[148:149], 0, s[4:5]
	s_add_i32 m0, s40, 0xc000
	ds_read_b128 v[200:203], v161
	ds_read_b128 v[204:207], v161 offset:1024
	ds_read_b128 v[208:211], v161 offset:2048
	ds_read_b128 v[212:215], v161 offset:3072
	ds_read_b128 v[216:219], v161 offset:4096
	ds_read_b128 v[220:223], v161 offset:5120
	ds_read_b128 v[224:227], v161 offset:6144
	ds_read_b128 v[228:231], v161 offset:7168
	global_load_lds_dwordx4 v[232:233], off
	v_lshl_add_u64 v[232:233], v[146:147], 0, s[4:5]
	s_add_i32 m0, s40, 0xe000
	s_nop 0
	global_load_lds_dwordx4 v[232:233], off
	s_waitcnt vmcnt(8)
	s_waitcnt lgkmcnt(0)
	s_setprio 1
	s_barrier
	v_mfma_f32_16x16x32_bf16 v[124:127], v[166:169], v[200:203], v[124:127]
	v_mfma_f32_16x16x32_bf16 v[120:123], v[174:177], v[200:203], v[120:123]
	v_mfma_f32_16x16x32_bf16 v[108:111], v[166:169], v[208:211], v[108:111]
	v_mfma_f32_16x16x32_bf16 v[104:107], v[174:177], v[208:211], v[104:107]
	v_mfma_f32_16x16x32_bf16 v[92:95], v[166:169], v[216:219], v[92:95]
	v_mfma_f32_16x16x32_bf16 v[88:91], v[174:177], v[216:219], v[88:91]
	v_mfma_f32_16x16x32_bf16 v[76:79], v[166:169], v[224:227], v[76:79]
	v_mfma_f32_16x16x32_bf16 v[72:75], v[174:177], v[224:227], v[72:75]
	v_mfma_f32_16x16x32_bf16 v[124:127], v[170:173], v[204:207], v[124:127]
	v_mfma_f32_16x16x32_bf16 v[120:123], v[178:181], v[204:207], v[120:123]
	v_mfma_f32_16x16x32_bf16 v[108:111], v[170:173], v[212:215], v[108:111]
	v_mfma_f32_16x16x32_bf16 v[104:107], v[178:181], v[212:215], v[104:107]
	v_mfma_f32_16x16x32_bf16 v[92:95], v[170:173], v[220:223], v[92:95]
	v_mfma_f32_16x16x32_bf16 v[88:91], v[178:181], v[220:223], v[88:91]
	v_mfma_f32_16x16x32_bf16 v[76:79], v[170:173], v[228:231], v[76:79]
	v_mfma_f32_16x16x32_bf16 v[72:75], v[178:181], v[228:231], v[72:75]
	v_mfma_f32_16x16x32_bf16 v[116:119], v[182:185], v[200:203], v[116:119]
	v_mfma_f32_16x16x32_bf16 v[112:115], v[190:193], v[200:203], v[112:115]
	v_mfma_f32_16x16x32_bf16 v[100:103], v[182:185], v[208:211], v[100:103]
	v_mfma_f32_16x16x32_bf16 v[96:99], v[190:193], v[208:211], v[96:99]
	v_mfma_f32_16x16x32_bf16 v[84:87], v[182:185], v[216:219], v[84:87]
	v_mfma_f32_16x16x32_bf16 v[80:83], v[190:193], v[216:219], v[80:83]
	v_mfma_f32_16x16x32_bf16 v[68:71], v[182:185], v[224:227], v[68:71]
	v_mfma_f32_16x16x32_bf16 v[64:67], v[190:193], v[224:227], v[64:67]
	v_mfma_f32_16x16x32_bf16 v[116:119], v[186:189], v[204:207], v[116:119]
	v_mfma_f32_16x16x32_bf16 v[112:115], v[194:197], v[204:207], v[112:115]
	v_mfma_f32_16x16x32_bf16 v[100:103], v[186:189], v[212:215], v[100:103]
	v_mfma_f32_16x16x32_bf16 v[96:99], v[194:197], v[212:215], v[96:99]
	v_mfma_f32_16x16x32_bf16 v[84:87], v[186:189], v[220:223], v[84:87]
	v_mfma_f32_16x16x32_bf16 v[80:83], v[194:197], v[220:223], v[80:83]
	v_mfma_f32_16x16x32_bf16 v[68:71], v[186:189], v[228:231], v[68:71]
	v_mfma_f32_16x16x32_bf16 v[64:67], v[194:197], v[228:231], v[64:67]
	s_setprio 0
	s_barrier
	s_add_i32 s62, s49, s39
	v_lshl_add_u64 v[232:233], s[34:35], 0, v[132:133]
	s_mov_b32 m0, s62
	ds_read_b128 v[200:203], v161 offset:16384
	ds_read_b128 v[204:207], v161 offset:17408
	ds_read_b128 v[208:211], v161 offset:18432
	ds_read_b128 v[212:215], v161 offset:19456
	ds_read_b128 v[216:219], v161 offset:20480
	ds_read_b128 v[220:223], v161 offset:21504
	ds_read_b128 v[224:227], v161 offset:22528
	ds_read_b128 v[228:231], v161 offset:23552
	global_load_lds_dwordx4 v[232:233], off
	v_lshl_add_u64 v[234:235], s[34:35], 0, v[134:135]
	s_add_i32 m0, s62, 0x2000
	s_add_i32 s34, s51, s39
	global_load_lds_dwordx4 v[234:235], off
	v_lshl_add_u64 v[236:237], s[30:31], 0, v[132:133]
	s_mov_b32 m0, s34
	v_lshl_add_u64 v[238:239], s[30:31], 0, v[134:135]
	global_load_lds_dwordx4 v[236:237], off
	s_add_i32 m0, s34, 0x2000
	v_mov_b32_e32 v139, v137
	global_load_lds_dwordx4 v[238:239], off
	s_mov_b32 m0, s40
	v_lshl_add_u64 v[240:241], s[6:7], 0, v[136:137]
	global_load_lds_dwordx4 v136, s[6:7]
	s_mov_b32 m0, s41
	v_lshl_add_u64 v[242:243], s[6:7], 0, v[138:139]
	global_load_lds_dwordx4 v138, s[6:7]
	s_waitcnt vmcnt(8)
	s_waitcnt lgkmcnt(0)
	s_setprio 1
	s_barrier
	v_mfma_f32_16x16x32_bf16 v[60:63], v[166:169], v[200:203], v[60:63]
	v_mfma_f32_16x16x32_bf16 v[56:59], v[174:177], v[200:203], v[56:59]
	v_mfma_f32_16x16x32_bf16 v[44:47], v[166:169], v[208:211], v[44:47]
	v_mfma_f32_16x16x32_bf16 v[40:43], v[174:177], v[208:211], v[40:43]
	v_mfma_f32_16x16x32_bf16 v[28:31], v[166:169], v[216:219], v[28:31]
	v_mfma_f32_16x16x32_bf16 v[24:27], v[174:177], v[216:219], v[24:27]
	v_mfma_f32_16x16x32_bf16 v[12:15], v[166:169], v[224:227], v[12:15]
	v_mfma_f32_16x16x32_bf16 v[8:11], v[174:177], v[224:227], v[8:11]
	v_mfma_f32_16x16x32_bf16 v[60:63], v[170:173], v[204:207], v[60:63]
	v_mfma_f32_16x16x32_bf16 v[56:59], v[178:181], v[204:207], v[56:59]
	v_mfma_f32_16x16x32_bf16 v[44:47], v[170:173], v[212:215], v[44:47]
	v_mfma_f32_16x16x32_bf16 v[40:43], v[178:181], v[212:215], v[40:43]
	v_mfma_f32_16x16x32_bf16 v[28:31], v[170:173], v[220:223], v[28:31]
	v_mfma_f32_16x16x32_bf16 v[24:27], v[178:181], v[220:223], v[24:27]
	v_mfma_f32_16x16x32_bf16 v[12:15], v[170:173], v[228:231], v[12:15]
	v_mfma_f32_16x16x32_bf16 v[8:11], v[178:181], v[228:231], v[8:11]
	v_mfma_f32_16x16x32_bf16 v[52:55], v[182:185], v[200:203], v[52:55]
	v_mfma_f32_16x16x32_bf16 v[48:51], v[190:193], v[200:203], v[48:51]
	v_mfma_f32_16x16x32_bf16 v[36:39], v[182:185], v[208:211], v[36:39]
	v_mfma_f32_16x16x32_bf16 v[32:35], v[190:193], v[208:211], v[32:35]
	v_mfma_f32_16x16x32_bf16 v[20:23], v[182:185], v[216:219], v[20:23]
	v_mfma_f32_16x16x32_bf16 v[16:19], v[190:193], v[216:219], v[16:19]
	v_mfma_f32_16x16x32_bf16 v[4:7], v[182:185], v[224:227], v[4:7]
	v_mfma_f32_16x16x32_bf16 v[0:3], v[190:193], v[224:227], v[0:3]
	v_mfma_f32_16x16x32_bf16 v[52:55], v[186:189], v[204:207], v[52:55]
	v_mfma_f32_16x16x32_bf16 v[48:51], v[194:197], v[204:207], v[48:51]
	v_mfma_f32_16x16x32_bf16 v[36:39], v[186:189], v[212:215], v[36:39]
	v_mfma_f32_16x16x32_bf16 v[32:35], v[194:197], v[212:215], v[32:35]
	v_mfma_f32_16x16x32_bf16 v[20:23], v[186:189], v[220:223], v[20:23]
	v_mfma_f32_16x16x32_bf16 v[16:19], v[194:197], v[220:223], v[16:19]
	v_mfma_f32_16x16x32_bf16 v[4:7], v[186:189], v[228:231], v[4:7]
	v_mfma_f32_16x16x32_bf16 v[0:3], v[194:197], v[228:231], v[0:3]
	s_setprio 0
	s_barrier
	s_add_i32 s30, 0, 0x18000
	ds_read_b128 v[166:169], v252 offset:32768
	ds_read_b128 v[170:173], v253 offset:32768
	s_add_i32 s31, 0, 0x1c000
	ds_read_b128 v[174:177], v252 offset:34816
	ds_read_b128 v[178:181], v253 offset:34816
	ds_read_b128 v[182:185], v252 offset:49152
	ds_read_b128 v[186:189], v253 offset:49152
	ds_read_b128 v[190:193], v252 offset:51200
	ds_read_b128 v[194:197], v253 offset:51200
	s_mov_b32 m0, s42
	v_lshl_add_u64 v[152:153], s[6:7], 0, v[152:153]
	ds_read_b128 v[200:203], v161 offset:32768
	ds_read_b128 v[204:207], v161 offset:33792
	ds_read_b128 v[208:211], v161 offset:34816
	ds_read_b128 v[212:215], v161 offset:35840
	ds_read_b128 v[216:219], v161 offset:36864
	ds_read_b128 v[220:223], v161 offset:37888
	ds_read_b128 v[224:227], v161 offset:38912
	ds_read_b128 v[228:231], v161 offset:39936
	global_load_lds_dwordx4 v[152:153], off
	v_lshl_add_u64 v[150:151], s[6:7], 0, v[150:151]
	s_mov_b32 m0, s43
	s_nop 0
	global_load_lds_dwordx4 v[150:151], off
	s_waitcnt vmcnt(8)
	s_waitcnt lgkmcnt(0)
	s_setprio 1
	s_barrier
	v_mfma_f32_16x16x32_bf16 v[124:127], v[166:169], v[200:203], v[124:127]
	v_mfma_f32_16x16x32_bf16 v[120:123], v[174:177], v[200:203], v[120:123]
	v_mfma_f32_16x16x32_bf16 v[108:111], v[166:169], v[208:211], v[108:111]
	v_mfma_f32_16x16x32_bf16 v[104:107], v[174:177], v[208:211], v[104:107]
	v_mfma_f32_16x16x32_bf16 v[92:95], v[166:169], v[216:219], v[92:95]
	v_mfma_f32_16x16x32_bf16 v[88:91], v[174:177], v[216:219], v[88:91]
	v_mfma_f32_16x16x32_bf16 v[76:79], v[166:169], v[224:227], v[76:79]
	v_mfma_f32_16x16x32_bf16 v[72:75], v[174:177], v[224:227], v[72:75]
	v_mfma_f32_16x16x32_bf16 v[124:127], v[170:173], v[204:207], v[124:127]
	v_mfma_f32_16x16x32_bf16 v[120:123], v[178:181], v[204:207], v[120:123]
	v_mfma_f32_16x16x32_bf16 v[108:111], v[170:173], v[212:215], v[108:111]
	v_mfma_f32_16x16x32_bf16 v[104:107], v[178:181], v[212:215], v[104:107]
	v_mfma_f32_16x16x32_bf16 v[92:95], v[170:173], v[220:223], v[92:95]
	v_mfma_f32_16x16x32_bf16 v[88:91], v[178:181], v[220:223], v[88:91]
	v_mfma_f32_16x16x32_bf16 v[76:79], v[170:173], v[228:231], v[76:79]
	v_mfma_f32_16x16x32_bf16 v[72:75], v[178:181], v[228:231], v[72:75]
	v_mfma_f32_16x16x32_bf16 v[116:119], v[182:185], v[200:203], v[116:119]
	v_mfma_f32_16x16x32_bf16 v[112:115], v[190:193], v[200:203], v[112:115]
	v_mfma_f32_16x16x32_bf16 v[100:103], v[182:185], v[208:211], v[100:103]
	v_mfma_f32_16x16x32_bf16 v[96:99], v[190:193], v[208:211], v[96:99]
	v_mfma_f32_16x16x32_bf16 v[84:87], v[182:185], v[216:219], v[84:87]
	v_mfma_f32_16x16x32_bf16 v[80:83], v[190:193], v[216:219], v[80:83]
	v_mfma_f32_16x16x32_bf16 v[68:71], v[182:185], v[224:227], v[68:71]
	v_mfma_f32_16x16x32_bf16 v[64:67], v[190:193], v[224:227], v[64:67]
	v_mfma_f32_16x16x32_bf16 v[116:119], v[186:189], v[204:207], v[116:119]
	v_mfma_f32_16x16x32_bf16 v[112:115], v[194:197], v[204:207], v[112:115]
	v_mfma_f32_16x16x32_bf16 v[100:103], v[186:189], v[212:215], v[100:103]
	v_mfma_f32_16x16x32_bf16 v[96:99], v[194:197], v[212:215], v[96:99]
	v_mfma_f32_16x16x32_bf16 v[84:87], v[186:189], v[220:223], v[84:87]
	v_mfma_f32_16x16x32_bf16 v[80:83], v[194:197], v[220:223], v[80:83]
	v_mfma_f32_16x16x32_bf16 v[68:71], v[186:189], v[228:231], v[68:71]
	v_mfma_f32_16x16x32_bf16 v[64:67], v[194:197], v[228:231], v[64:67]
	s_setprio 0
	s_barrier
	s_add_i32 s6, s30, s39
	v_lshl_add_u64 v[228:229], v[232:233], 0, s[20:21]
	s_mov_b32 m0, s6
	ds_read_b128 v[150:153], v161 offset:49152
	ds_read_b128 v[200:203], v161 offset:50176
	ds_read_b128 v[204:207], v161 offset:51200
	ds_read_b128 v[208:211], v161 offset:52224
	ds_read_b128 v[212:215], v161 offset:53248
	ds_read_b128 v[216:219], v161 offset:54272
	ds_read_b128 v[220:223], v161 offset:55296
	ds_read_b128 v[224:227], v161 offset:56320
	global_load_lds_dwordx4 v[228:229], off
	v_lshl_add_u64 v[228:229], v[234:235], 0, s[20:21]
	s_add_i32 m0, s6, 0x2000
	s_add_i32 s6, s31, s39
	global_load_lds_dwordx4 v[228:229], off
	v_lshl_add_u64 v[228:229], v[236:237], 0, s[20:21]
	s_mov_b32 m0, s6
	s_nop 0
	global_load_lds_dwordx4 v[228:229], off
	v_lshl_add_u64 v[228:229], v[238:239], 0, s[20:21]
	s_add_i32 m0, s6, 0x2000
	s_nop 0
	global_load_lds_dwordx4 v[228:229], off
	v_lshl_add_u64 v[228:229], v[240:241], 0, s[20:21]
	s_mov_b32 m0, s47
	s_nop 0
	global_load_lds_dwordx4 v[228:229], off
	v_lshl_add_u64 v[228:229], v[242:243], 0, s[20:21]
	s_mov_b32 m0, s48
	s_nop 0
	global_load_lds_dwordx4 v[228:229], off
	s_waitcnt vmcnt(8)
	s_waitcnt lgkmcnt(0)
	s_setprio 1
	s_barrier
	v_mfma_f32_16x16x32_bf16 v[60:63], v[166:169], v[150:153], v[60:63]
	v_mfma_f32_16x16x32_bf16 v[56:59], v[174:177], v[150:153], v[56:59]
	v_mfma_f32_16x16x32_bf16 v[44:47], v[166:169], v[204:207], v[44:47]
	v_mfma_f32_16x16x32_bf16 v[40:43], v[174:177], v[204:207], v[40:43]
	v_mfma_f32_16x16x32_bf16 v[28:31], v[166:169], v[212:215], v[28:31]
	v_mfma_f32_16x16x32_bf16 v[24:27], v[174:177], v[212:215], v[24:27]
	v_mfma_f32_16x16x32_bf16 v[12:15], v[166:169], v[220:223], v[12:15]
	v_mfma_f32_16x16x32_bf16 v[8:11], v[174:177], v[220:223], v[8:11]
	v_mfma_f32_16x16x32_bf16 v[60:63], v[170:173], v[200:203], v[60:63]
	v_mfma_f32_16x16x32_bf16 v[56:59], v[178:181], v[200:203], v[56:59]
	v_mfma_f32_16x16x32_bf16 v[44:47], v[170:173], v[208:211], v[44:47]
	v_mfma_f32_16x16x32_bf16 v[40:43], v[178:181], v[208:211], v[40:43]
	v_mfma_f32_16x16x32_bf16 v[28:31], v[170:173], v[216:219], v[28:31]
	v_mfma_f32_16x16x32_bf16 v[24:27], v[178:181], v[216:219], v[24:27]
	v_mfma_f32_16x16x32_bf16 v[12:15], v[170:173], v[224:227], v[12:15]
	v_mfma_f32_16x16x32_bf16 v[8:11], v[178:181], v[224:227], v[8:11]
	v_mfma_f32_16x16x32_bf16 v[52:55], v[182:185], v[150:153], v[52:55]
	v_mfma_f32_16x16x32_bf16 v[48:51], v[190:193], v[150:153], v[48:51]
	v_mfma_f32_16x16x32_bf16 v[36:39], v[182:185], v[204:207], v[36:39]
	v_mfma_f32_16x16x32_bf16 v[32:35], v[190:193], v[204:207], v[32:35]
	v_mfma_f32_16x16x32_bf16 v[20:23], v[182:185], v[212:215], v[20:23]
	v_mfma_f32_16x16x32_bf16 v[16:19], v[190:193], v[212:215], v[16:19]
	v_mfma_f32_16x16x32_bf16 v[4:7], v[182:185], v[220:223], v[4:7]
	v_mfma_f32_16x16x32_bf16 v[0:3], v[190:193], v[220:223], v[0:3]
	v_mfma_f32_16x16x32_bf16 v[52:55], v[186:189], v[200:203], v[52:55]
	v_mfma_f32_16x16x32_bf16 v[48:51], v[194:197], v[200:203], v[48:51]
	v_mfma_f32_16x16x32_bf16 v[36:39], v[186:189], v[208:211], v[36:39]
	v_mfma_f32_16x16x32_bf16 v[32:35], v[194:197], v[208:211], v[32:35]
	v_mfma_f32_16x16x32_bf16 v[20:23], v[186:189], v[216:219], v[20:23]
	v_mfma_f32_16x16x32_bf16 v[16:19], v[194:197], v[216:219], v[16:19]
	v_mfma_f32_16x16x32_bf16 v[4:7], v[186:189], v[224:227], v[4:7]
	v_mfma_f32_16x16x32_bf16 v[0:3], v[194:197], v[224:227], v[0:3]
	s_setprio 0
	s_barrier
	s_add_i32 s61, s61, 2
	s_add_u32 s4, s4, 0x100
	s_addc_u32 s5, s5, 0
	s_cmp_gt_u32 s61, 13
	s_cbranch_scc1 .LBB0_842

.LBB0_1549:
	s_add_u32 s26, s4, s24
	s_addc_u32 s27, s5, s25
	s_add_u32 s28, s26, 0x28000100
	s_addc_u32 s29, s27, 0
	ds_read_b128 v[24:27], v252
	ds_read_b128 v[28:31], v253
	s_and_b64 s[26:27], s[30:31], exec
	ds_read_b128 v[16:19], v252 offset:2048
	ds_read_b128 v[20:23], v253 offset:2048
	s_cselect_b32 s27, s7, s29
	s_cselect_b32 s26, s6, s28
	s_add_u32 s63, s58, s24
	ds_read_b128 v[8:11], v252 offset:16384
	ds_read_b128 v[12:15], v253 offset:16384
	s_addc_u32 s64, s59, s25
	ds_read_b128 v[0:3], v252 offset:18432
	ds_read_b128 v[4:7], v253 offset:18432
	s_and_b64 s[28:29], s[30:31], exec
	s_cselect_b32 s29, s21, s64
	s_cselect_b32 s28, s20, s63
	s_add_u32 s63, s60, s24
	s_addc_u32 s64, s61, s25
	s_and_b64 s[30:31], s[30:31], exec
	s_cselect_b32 s31, s23, s64
	s_cselect_b32 s30, s22, s63
	s_add_u32 s100, s14, s24
	s_addc_u32 s101, s15, s25
	s_add_i32 m0, s35, 0xc000
	ds_read_b128 v[186:189], v206
	ds_read_b128 v[214:217], v206 offset:2048
	ds_read_b128 v[190:193], v207
	ds_read_b128 v[218:221], v207 offset:2048
	ds_read_b128 v[222:225], v206 offset:4096
	ds_read_b128 v[230:233], v206 offset:6144
	ds_read_b128 v[226:229], v207 offset:4096
	ds_read_b128 v[234:237], v207 offset:6144
	global_load_lds_dwordx4 v168, s[100:101]
	s_add_i32 m0, s35, 0xe000
	s_nop 0
	global_load_lds_dwordx4 v170, s[100:101]
	s_waitcnt vmcnt(8)
	s_waitcnt lgkmcnt(0)
	s_setprio 1
	s_barrier
	s_cmp_eq_u32 s24, 0
	s_cbranch_scc1 .Lc0_P12_0
	v_mfma_f32_16x16x128_f8f6f4 v[156:159], v[24:31], v[186:193], v[156:159]
	v_mfma_f32_16x16x128_f8f6f4 v[152:155], v[16:23], v[186:193], v[152:155]
	v_mfma_f32_16x16x128_f8f6f4 v[136:139], v[16:23], v[214:221], v[136:139]
	v_mfma_f32_16x16x128_f8f6f4 v[144:147], v[24:31], v[214:221], v[144:147]
	v_mfma_f32_16x16x128_f8f6f4 v[124:127], v[24:31], v[222:229], v[124:127]
	v_mfma_f32_16x16x128_f8f6f4 v[120:123], v[16:23], v[222:229], v[120:123]
	v_mfma_f32_16x16x128_f8f6f4 v[104:107], v[16:23], v[230:237], v[104:107]
	v_mfma_f32_16x16x128_f8f6f4 v[112:115], v[24:31], v[230:237], v[112:115]
	v_mfma_f32_16x16x128_f8f6f4 v[148:151], v[8:15], v[186:193], v[148:151]
	v_mfma_f32_16x16x128_f8f6f4 v[140:143], v[0:7], v[186:193], v[140:143]
	v_mfma_f32_16x16x128_f8f6f4 v[128:131], v[0:7], v[214:221], v[128:131]
	v_mfma_f32_16x16x128_f8f6f4 v[132:135], v[8:15], v[214:221], v[132:135]
	v_mfma_f32_16x16x128_f8f6f4 v[116:119], v[8:15], v[222:229], v[116:119]
	v_mfma_f32_16x16x128_f8f6f4 v[108:111], v[0:7], v[222:229], v[108:111]
	v_mfma_f32_16x16x128_f8f6f4 v[96:99], v[0:7], v[230:237], v[96:99]
	v_mfma_f32_16x16x128_f8f6f4 v[100:103], v[8:15], v[230:237], v[100:103]
.Lc0b_P12_0:
	s_setprio 0
	s_barrier
	s_add_i32 s63, s46, s34
	s_mov_b32 m0, s63
	ds_read_b128 v[214:217], v206 offset:16384
	ds_read_b128 v[222:225], v206 offset:18432
	ds_read_b128 v[218:221], v207 offset:16384
	ds_read_b128 v[226:229], v207 offset:18432
	ds_read_b128 v[230:233], v206 offset:20480
	ds_read_b128 v[238:241], v206 offset:22528
	ds_read_b128 v[234:237], v207 offset:20480
	ds_read_b128 v[242:245], v207 offset:22528
	global_load_lds_dwordx4 v160, s[28:29]
	s_add_i32 m0, s63, 0x2000
	s_add_i32 s98, s48, s34
	global_load_lds_dwordx4 v162, s[28:29]
	s_mov_b32 m0, s98
	s_nop 0
	global_load_lds_dwordx4 v160, s[30:31]
	s_add_i32 m0, s98, 0x2000
	v_mov_b32_e32 v167, v165
	global_load_lds_dwordx4 v162, s[30:31]
	s_waitcnt vmcnt(6)
	s_waitcnt lgkmcnt(0)
	s_setprio 1
	s_barrier
	s_cmp_eq_u32 s24, 0
	s_cbranch_scc1 .Lc0_P12_1
	v_mfma_f32_16x16x128_f8f6f4 v[92:95], v[24:31], v[214:221], v[92:95]
	v_mfma_f32_16x16x128_f8f6f4 v[88:91], v[16:23], v[214:221], v[88:91]
	v_mfma_f32_16x16x128_f8f6f4 v[72:75], v[16:23], v[222:229], v[72:75]
	v_mfma_f32_16x16x128_f8f6f4 v[80:83], v[24:31], v[222:229], v[80:83]
	s_mov_b32 m0, s35
	v_mfma_f32_16x16x128_f8f6f4 v[60:63], v[24:31], v[230:237], v[60:63]
	global_load_lds_dwordx4 v164, s[26:27]
	v_mfma_f32_16x16x128_f8f6f4 v[56:59], v[16:23], v[230:237], v[56:59]
	v_mfma_f32_16x16x128_f8f6f4 v[40:43], v[16:23], v[238:245], v[40:43]
	v_mfma_f32_16x16x128_f8f6f4 v[48:51], v[24:31], v[238:245], v[48:51]
	v_mfma_f32_16x16x128_f8f6f4 v[84:87], v[8:15], v[214:221], v[84:87]
	s_mov_b32 m0, s36
	v_mfma_f32_16x16x128_f8f6f4 v[76:79], v[0:7], v[214:221], v[76:79]
	global_load_lds_dwordx4 v166, s[26:27]
	v_mfma_f32_16x16x128_f8f6f4 v[64:67], v[0:7], v[222:229], v[64:67]
	v_mfma_f32_16x16x128_f8f6f4 v[68:71], v[8:15], v[222:229], v[68:71]
	v_mfma_f32_16x16x128_f8f6f4 v[52:55], v[8:15], v[230:237], v[52:55]
	v_mfma_f32_16x16x128_f8f6f4 v[44:47], v[0:7], v[230:237], v[44:47]
	v_mfma_f32_16x16x128_f8f6f4 v[32:35], v[0:7], v[238:245], v[32:35]
	v_mfma_f32_16x16x128_f8f6f4 v[36:39], v[8:15], v[238:245], v[36:39]
.Lc0b_P12_1:
	s_setprio 0
	s_barrier
	ds_read_b128 v[0:3], v252 offset:32768
	ds_read_b128 v[4:7], v253 offset:32768
	ds_read_b128 v[8:11], v252 offset:34816
	ds_read_b128 v[12:15], v253 offset:34816
	ds_read_b128 v[16:19], v252 offset:49152
	ds_read_b128 v[20:23], v253 offset:49152
	ds_read_b128 v[24:27], v252 offset:51200
	ds_read_b128 v[28:31], v253 offset:51200
	s_mov_b32 m0, s37
	ds_read_b128 v[214:217], v206 offset:32768
	ds_read_b128 v[222:225], v206 offset:34816
	ds_read_b128 v[218:221], v207 offset:32768
	ds_read_b128 v[226:229], v207 offset:34816
	ds_read_b128 v[230:233], v206 offset:36864
	ds_read_b128 v[238:241], v206 offset:38912
	ds_read_b128 v[234:237], v207 offset:36864
	ds_read_b128 v[242:245], v207 offset:38912
	global_load_lds_dwordx4 v184, s[26:27]
	s_mov_b32 m0, s38
	s_nop 0
	global_load_lds_dwordx4 v182, s[26:27]
	s_waitcnt vmcnt(8)
	s_waitcnt lgkmcnt(0)
	s_setprio 1
	s_barrier
	v_mfma_f32_16x16x128_f8f6f4 v[156:159], v[0:7], v[214:221], v[156:159]
	v_mfma_f32_16x16x128_f8f6f4 v[152:155], v[8:15], v[214:221], v[152:155]
	v_mfma_f32_16x16x128_f8f6f4 v[136:139], v[8:15], v[222:229], v[136:139]
	v_mfma_f32_16x16x128_f8f6f4 v[144:147], v[0:7], v[222:229], v[144:147]
	v_mfma_f32_16x16x128_f8f6f4 v[124:127], v[0:7], v[230:237], v[124:127]
	v_mfma_f32_16x16x128_f8f6f4 v[120:123], v[8:15], v[230:237], v[120:123]
	v_mfma_f32_16x16x128_f8f6f4 v[104:107], v[8:15], v[238:245], v[104:107]
	v_mfma_f32_16x16x128_f8f6f4 v[112:115], v[0:7], v[238:245], v[112:115]
	v_mfma_f32_16x16x128_f8f6f4 v[148:151], v[16:23], v[214:221], v[148:151]
	v_mfma_f32_16x16x128_f8f6f4 v[140:143], v[24:31], v[214:221], v[140:143]
	v_mfma_f32_16x16x128_f8f6f4 v[128:131], v[24:31], v[222:229], v[128:131]
	v_mfma_f32_16x16x128_f8f6f4 v[132:135], v[16:23], v[222:229], v[132:135]
	v_mfma_f32_16x16x128_f8f6f4 v[116:119], v[16:23], v[230:237], v[116:119]
	v_mfma_f32_16x16x128_f8f6f4 v[108:111], v[24:31], v[230:237], v[108:111]
	v_mfma_f32_16x16x128_f8f6f4 v[96:99], v[24:31], v[238:245], v[96:99]
	v_mfma_f32_16x16x128_f8f6f4 v[100:103], v[16:23], v[238:245], v[100:103]
	s_setprio 0
	s_barrier
	s_add_i32 s99, s34, 0x17f80
	s_mov_b32 m0, s99
	ds_read_b128 v[214:217], v206 offset:49152
	ds_read_b128 v[222:225], v206 offset:51200
	ds_read_b128 v[218:221], v207 offset:49152
	ds_read_b128 v[226:229], v207 offset:51200
	ds_read_b128 v[230:233], v206 offset:53248
	ds_read_b128 v[238:241], v206 offset:55296
	ds_read_b128 v[234:237], v207 offset:53248
	ds_read_b128 v[242:245], v207 offset:55296
	global_load_lds_dwordx4 v160, s[28:29] offset:128
	s_add_i32 m0, s99, 0x2000
	s_add_i32 s99, s34, 0x1bf80
	global_load_lds_dwordx4 v162, s[28:29] offset:128
	s_mov_b32 m0, s99
	s_nop 0
	global_load_lds_dwordx4 v160, s[30:31] offset:128
	s_add_i32 m0, s99, 0x2000
	s_nop 0
	global_load_lds_dwordx4 v162, s[30:31] offset:128
	s_waitcnt vmcnt(6)
	s_waitcnt lgkmcnt(0)
	s_setprio 1
	s_barrier
	v_mfma_f32_16x16x128_f8f6f4 v[92:95], v[0:7], v[214:221], v[92:95]
	v_mfma_f32_16x16x128_f8f6f4 v[88:91], v[8:15], v[214:221], v[88:91]
	v_mfma_f32_16x16x128_f8f6f4 v[72:75], v[8:15], v[222:229], v[72:75]
	v_mfma_f32_16x16x128_f8f6f4 v[80:83], v[0:7], v[222:229], v[80:83]
	s_add_i32 m0, s41, 0xffffff80
	v_mfma_f32_16x16x128_f8f6f4 v[60:63], v[0:7], v[230:237], v[60:63]
	global_load_lds_dwordx4 v164, s[26:27] offset:128
	v_mfma_f32_16x16x128_f8f6f4 v[56:59], v[8:15], v[230:237], v[56:59]
	v_mfma_f32_16x16x128_f8f6f4 v[40:43], v[8:15], v[238:245], v[40:43]
	v_mfma_f32_16x16x128_f8f6f4 v[48:51], v[0:7], v[238:245], v[48:51]
	v_mfma_f32_16x16x128_f8f6f4 v[84:87], v[16:23], v[214:221], v[84:87]
	s_add_i32 m0, s42, 0xffffff80
	v_mfma_f32_16x16x128_f8f6f4 v[76:79], v[24:31], v[214:221], v[76:79]
	global_load_lds_dwordx4 v166, s[26:27] offset:128
	v_mfma_f32_16x16x128_f8f6f4 v[64:67], v[24:31], v[222:229], v[64:67]
	v_mfma_f32_16x16x128_f8f6f4 v[68:71], v[16:23], v[222:229], v[68:71]
	v_mfma_f32_16x16x128_f8f6f4 v[52:55], v[16:23], v[230:237], v[52:55]
	v_mfma_f32_16x16x128_f8f6f4 v[44:47], v[24:31], v[230:237], v[44:47]
	v_mfma_f32_16x16x128_f8f6f4 v[32:35], v[24:31], v[238:245], v[32:35]
	v_mfma_f32_16x16x128_f8f6f4 v[36:39], v[16:23], v[238:245], v[36:39]
	s_setprio 0
	s_barrier
	s_add_i32 s62, s62, 2
	s_add_u32 s24, s24, 0x100
	s_addc_u32 s25, s25, 0
	s_cmp_gt_u32 s62, 29
	s_cbranch_scc1 .LBB0_1552
